# speedup vs baseline: 1.0415x; 1.0085x over previous
_Z6k_attnILi1024ELi1024ELi1024ELi1024ELi3072ELi1024ELb1ELb1EEvPKDF16_S1_S1_PKfPDF16_:
	s_load_dwordx8 s[8:15], s[0:1], 0x0
	s_load_dwordx2 s[16:17], s[0:1], 0x20
	s_lshl_b32 s0, s2, 1
	s_and_b32 s24, s0, 14
	s_lshr_b32 s0, s2, 7
	s_add_i32 s24, s24, s0
	v_readfirstlane_b32 s40, v0
	s_lshr_b32 s0, s24, 2
	s_lshr_b32 s33, s40, 6
	s_mov_b32 s1, 0
	s_lshl_b32 s3, s2, 3
	s_lshr_b32 s4, s40, 2
	s_lshr_b32 s55, s2, 3
	s_and_b32 s55, s55, 7
	s_lshl_b32 s55, s55, 1
	s_lshr_b32 s6, s33, 2
	s_add_i32 s6, s6, s55
	s_lshl_b32 s6, s6, 6
	s_lshr_b32 s57, s33, 2
	s_lshl_b32 s57, s57, 12
	s_lshr_b32 s61, s33, 2
	s_mul_i32 s61, s61, 0x6800
	s_mov_b64 s[58:59], 0x80
	s_lshl_b64 s[20:21], s[0:1], 20
	s_and_b32 s3, s4, 48
	s_lshl_b32 s35, s33, 10
	s_cmp_lg_u32 0, -1
	s_cselect_b32 s5, 0, 0
	s_add_i32 s37, s35, s5
	s_waitcnt lgkmcnt(0)
	s_add_u32 s5, s10, s20
	v_bfe_u32 v202, v0, 2, 4
	s_addc_u32 s19, s11, s21
	v_or_b32_e32 v20, s3, v202
	s_add_u32 s18, s5, s6
	v_bfe_u32 v30, v0, 4, 2
	s_addc_u32 s19, s19, 0
	v_lshlrev_b32_e32 v18, 10, v20
	v_mov_b32_e32 v19, 0
	v_bitop3_b32 v1, v30, v0, 3 bitop3:0x78
	v_lshl_add_u64 v[2:3], s[18:19], 0, v[18:19]
	v_lshlrev_b32_e32 v18, 4, v1
	s_cmpk_lt_u32 s40, 0x100
	s_mov_b32 s7, s1
	v_and_b32_e32 v24, 3, v0
	s_cselect_b64 s[18:19], -1, 0
	s_cmpk_gt_u32 s40, 0xff
	v_lshl_add_u64 v[22:23], v[2:3], 0, v[18:19]
	s_nop 0
	s_mov_b32 m0, s37
	s_nop 0
	global_load_lds_dwordx4 v[22:23], off
.LBB3_2:
	s_mul_i32 s46, s0, 0x600000
	s_mul_hi_u32 s45, s0, 0x600000
	s_add_u32 s5, s12, s46
	s_addc_u32 s23, s13, s45
	s_lshl_b32 s22, s55, 7
	s_add_u32 s22, s5, s22
	s_addc_u32 s23, s23, 0
	s_movk_i32 s5, 0x1800
	v_mov_b64_e32 v[2:3], s[22:23]
	v_mad_u64_u32 v[2:3], s[22:23], v20, s5, v[2:3]
	s_and_b32 s22, s4, 0x3fffffc0
	s_cmp_lg_u32 0, -1
	s_mov_b32 s23, s1
	s_cselect_b32 s4, 0, 0
	v_lshl_add_u64 v[2:3], v[2:3], 0, s[22:23]
	v_lshlrev_b32_e32 v160, 4, v24
	v_mov_b32_e32 v161, v19
	s_add_i32 s4, s4, s35
	v_lshl_add_u64 v[162:163], v[2:3], 0, v[160:161]
	s_add_i32 s34, s4, 0x6000
	v_cndmask_b32_e64 v2, 0, 1, s[18:19]
	s_andn2_b64 vcc, exec, s[18:19]
	s_mov_b32 m0, s34
	s_nop 0
	global_load_lds_dwordx4 v[162:163], off
	v_lshl_add_u64 v[226:227], v[162:163], 0, s[58:59]
	s_add_i32 m0, s34, 0x6800
	s_nop 0
	global_load_lds_dwordx4 v[226:227], off
	v_and_b32_e32 v1, 63, v0
	v_cmp_ne_u32_e64 s[4:5], 1, v2
	s_nop 0
	s_mov_b64 s[18:19], 0x10000
	s_cmp_lg_u32 0, -1
	v_lshl_add_u64 v[2:3], v[22:23], 0, s[18:19]
	s_cselect_b32 s18, 0, 0
	s_add_i32 s18, s18, s35
	s_addk_i32 s18, 0x2000
	s_mov_b32 m0, s18
	s_nop 0
	global_load_lds_dwordx4 v[2:3], off
.LBB3_4:
	s_lshl_b32 s18, s24, 8
	s_and_b32 s18, s18, 0x300
	s_lshl_b64 s[0:1], s[0:1], 10
	s_or_b32 s0, s0, s18
	s_lshr_b32 s56, s2, 6
	s_and_b32 s56, s56, 1
	s_lshl_b32 s56, s56, 2
	s_and_b32 s18, s33, 3
	s_or_b32 s18, s18, s56
	s_lshl_b32 s18, s18, 5
	s_add_u32 s18, s0, s18
	v_and_b32_e32 v203, 31, v0
	s_addc_u32 s19, s1, 0
	v_or_b32_e32 v2, s18, v203
	v_mov_b32_e32 v3, s19
	v_lshrrev_b32_e32 v204, 5, v1
	v_lshlrev_b64 v[4:5], 10, v[2:3]
	v_lshlrev_b64 v[2:3], 12, v[2:3]
	v_lshl_add_u64 v[2:3], s[14:15], 0, v[2:3]
	v_lshlrev_b32_e32 v28, 4, v204
	v_mov_b32_e32 v29, 0
	v_lshl_add_u64 v[26:27], v[2:3], 0, v[28:29]
	v_lshl_add_u64 v[2:3], s[8:9], 0, v[4:5]
	v_lshl_add_u64 v[2:3], v[2:3], 0, s[6:7]
	v_and_b32_e32 v28, 32, v0
	v_lshl_add_u64 v[40:41], v[2:3], 0, v[28:29]
	global_load_dwordx4 v[100:103], v[40:41], off offset:16
	global_load_dwordx4 v[96:99], v[40:41], off
	v_mul_hi_u32_u24_e32 v21, 0x1800, v20
	s_and_b64 vcc, exec, s[4:5]
	v_mul_u32_u24_e32 v20, 0x1800, v20
	s_nop 0
	s_mov_b64 s[0:1], 0x20000
	s_cmp_lg_u32 0, -1
	v_lshl_add_u64 v[26:27], v[22:23], 0, s[0:1]
	s_cselect_b32 s0, 0, 0
	s_add_i32 s0, s0, s35
	s_addk_i32 s0, 0x4000
	s_mov_b32 m0, s0
	s_nop 0
	global_load_lds_dwordx4 v[26:27], off
.LBB3_6:
	v_lshlrev_b32_e32 v104, 3, v24
	v_or_b32_e32 v24, s18, v30
	v_mov_b32_e32 v25, s19
	v_lshlrev_b64 v[24:25], 12, v[24:25]
	v_lshl_add_u64 v[80:81], s[14:15], 0, v[24:25]
	v_lshrrev_b32_e32 v106, 2, v203
	v_lshlrev_b32_e32 v24, 1, v204
	v_bfe_u32 v25, v203, 2, 2
	s_and_b32 s7, s33, 3
	s_lshl_b32 s7, s7, 13
	s_lshr_b32 s62, s33, 2
	s_lshl_b32 s62, s62, 16
	s_mov_b32 s63, 0
	s_lshr_b32 s64, s33, 2
	s_lshl_b32 s64, s64, 12
	s_add_i32 s65, s64, 0x8000
	v_bitop3_b32 v26, v24, v106, 3 bitop3:0x78
	v_bitop3_b32 v24, v24, v25, 1 bitop3:0x36
	s_cmp_lg_u32 0, -1
	v_lshlrev_b32_e32 v218, 4, v24
	v_bitop3_b32 v24, v30, v0, 15 bitop3:0x78
	s_cselect_b32 s0, 0, 0
	v_lshlrev_b32_e32 v28, 4, v24
	s_add_i32 s23, s0, s7
	v_lshl_add_u64 v[164:165], v[80:81], 0, v[28:29]
	s_mov_b64 s[0:1], 0x0
	v_and_b32_e32 v105, 15, v0
	v_lshl_add_u64 v[24:25], v[164:165], 0, s[0:1]
	v_lshl_add_u64 v[24:25], v[24:25], 0, s[62:63]
	s_add_i32 s36, s23, 0x14800
	s_add_i32 m0, s36, s64
	s_nop 0
	global_load_lds_dwordx4 v[24:25], off nt
	v_bitop3_b32 v24, v30, v105, 4 bitop3:0x36
	v_lshlrev_b32_e32 v28, 4, v24
	v_lshl_add_u64 v[24:25], v[80:81], 0, v[28:29]
	s_mov_b64 s[8:9], 0x4000
	v_lshlrev_b32_e32 v217, 4, v26
	v_lshl_add_u64 v[26:27], v[24:25], 0, s[8:9]
	v_lshl_add_u64 v[26:27], v[26:27], 0, s[62:63]
	s_add_i32 s8, s23, 0x14c00
	s_add_i32 m0, s8, s64
	s_nop 0
	global_load_lds_dwordx4 v[26:27], off nt
	v_bitop3_b32 v26, v30, v105, 8 bitop3:0x36
	v_lshlrev_b32_e32 v28, 4, v26
	v_lshl_add_u64 v[26:27], v[80:81], 0, v[28:29]
	s_mov_b64 s[14:15], 0x8000
	v_bitop3_b32 v28, v30, v105, 12 bitop3:0x36
	v_lshl_add_u64 v[82:83], v[26:27], 0, s[14:15]
	v_lshl_add_u64 v[82:83], v[82:83], 0, s[62:63]
	s_add_i32 s14, s23, 0x15000
	s_add_i32 m0, s14, s64
	s_nop 0
	global_load_lds_dwordx4 v[82:83], off nt
	v_lshlrev_b32_e32 v28, 4, v28
	v_lshl_add_u64 v[28:29], v[80:81], 0, v[28:29]
	s_mov_b64 s[14:15], 0xc000
	v_lshl_add_u64 v[80:81], v[28:29], 0, s[14:15]
	v_lshl_add_u64 v[80:81], v[80:81], 0, s[62:63]
	s_add_i32 s14, s23, 0x15400
	s_add_i32 m0, s14, s64
	s_nop 0
	global_load_lds_dwordx4 v[80:81], off nt
	s_mov_b64 s[26:27], 0x10000
	s_add_i32 s26, s23, 0x15800
	s_mov_b64 s[28:29], 0x14000
	s_add_i32 s28, s23, 0x15c00
	s_mov_b64 s[30:31], 0x18000
	s_add_i32 s30, s23, 0x16000
	s_mov_b64 s[30:31], 0x1c000
	v_lshl_add_u32 v216, v203, 6, 0
	v_add_u32_e32 v216, s57, v216
	s_add_i32 s23, s23, 0x16400
	s_waitcnt vmcnt(0) lgkmcnt(0)
	s_barrier
	v_and_b32_e32 v226, 31, v0
	v_bfe_u32 v227, v0, 5, 1
	v_lshrrev_b32_e32 v228, 2, v226
	v_lshlrev_b32_e32 v228, 10, v228
	v_and_b32_e32 v229, 3, v226
	v_lshlrev_b32_e32 v229, 8, v229
	v_add3_u32 v230, s36, v228, v229
	v_and_b32_e32 v231, 15, v226
	v_xor_b32_e32 v231, v231, v227
	v_lshlrev_b32_e32 v231, 4, v231
	v_mov_b32_e32 v232, v231
	v_add_u32_e32 v232, v230, v232
	ds_read_b128 v[64:67], v232
	v_xor_b32_e32 v233, 0x80, v231
	v_add_u32_e32 v233, v230, v233
	ds_read_b128 v[2:5], v233
	v_xor_b32_e32 v234, 0x20, v231
	v_add_u32_e32 v234, v230, v234
	ds_read_b128 v[68:71], v234
	v_xor_b32_e32 v235, 0xa0, v231
	v_add_u32_e32 v235, v230, v235
	ds_read_b128 v[6:9], v235
	v_xor_b32_e32 v236, 0x40, v231
	v_add_u32_e32 v236, v230, v236
	ds_read_b128 v[72:75], v236
	v_xor_b32_e32 v237, 0xc0, v231
	v_add_u32_e32 v237, v230, v237
	ds_read_b128 v[10:13], v237
	v_xor_b32_e32 v238, 0x60, v231
	v_add_u32_e32 v238, v230, v238
	ds_read_b128 v[76:79], v238
	v_xor_b32_e32 v239, 0xe0, v231
	v_add_u32_e32 v239, v230, v239
	ds_read_b128 v[14:17], v239
	s_waitcnt lgkmcnt(0)
	s_mov_b64 s[52:53], 0x100
	v_lshl_add_u64 v[224:225], v[164:165], 0, s[52:53]
	v_lshl_add_u64 v[224:225], v[224:225], 0, s[62:63]
	s_add_i32 s54, s36, 0x0
	s_add_i32 m0, s54, s65
	s_nop 0
	global_load_lds_dwordx4 v[224:225], off nt
	s_mov_b64 s[52:53], 0x4100
	v_lshl_add_u64 v[224:225], v[24:25], 0, s[52:53]
	v_lshl_add_u64 v[224:225], v[224:225], 0, s[62:63]
	s_add_i32 s54, s36, 0x400
	s_add_i32 m0, s54, s65
	s_nop 0
	global_load_lds_dwordx4 v[224:225], off nt
	s_mov_b64 s[52:53], 0x8100
	v_lshl_add_u64 v[224:225], v[26:27], 0, s[52:53]
	v_lshl_add_u64 v[224:225], v[224:225], 0, s[62:63]
	s_add_i32 s54, s36, 0x800
	s_add_i32 m0, s54, s65
	s_nop 0
	global_load_lds_dwordx4 v[224:225], off nt
	s_mov_b64 s[52:53], 0xc100
	v_lshl_add_u64 v[224:225], v[28:29], 0, s[52:53]
	v_lshl_add_u64 v[224:225], v[224:225], 0, s[62:63]
	s_add_i32 s54, s36, 0xc00
	s_add_i32 m0, s54, s65
	s_nop 0
	global_load_lds_dwordx4 v[224:225], off nt
	s_mov_b64 s[52:53], 0x10100
	s_add_i32 s54, s36, 0x1000
	s_mov_b64 s[52:53], 0x14100
	s_add_i32 s54, s36, 0x1400
	s_mov_b64 s[52:53], 0x18100
	s_add_i32 s54, s36, 0x1800
	s_mov_b64 s[52:53], 0x1c100
	s_add_i32 s54, s36, 0x1c00
	v_add_u32_e32 v209, v216, v217
	v_add_u32_e32 v210, v216, v218
	ds_read_b128 v[80:83], v209
	ds_read_b128 v[88:91], v209 offset:2048
	ds_read_b128 v[84:87], v210
	ds_read_b128 v[92:95], v210 offset:2048
	v_mov_b32_e32 v219, 0x7f7f7f7f
	v_mov_b32_e32 v220, 0x7c7c7c7c
	s_waitcnt vmcnt(10) lgkmcnt(1)
	v_mfma_scale_f32_32x32x64_f8f6f4 v[64:79], v[80:87], v[96:103], v[64:79], v219, v220 op_sel_hi:[0,0,0]
	s_waitcnt vmcnt(8) lgkmcnt(0)
	v_mfma_scale_f32_32x32x64_f8f6f4 v[2:17], v[88:95], v[96:103], v[2:17], v219, v220 op_sel_hi:[0,0,0]
	s_mov_b32 s39, 0x3fb8aa3b
	s_nop 15
	s_nop 15
	s_nop 15
	s_nop 15
	s_nop 15
	s_nop 15
	s_waitcnt vmcnt(0) lgkmcnt(0)
	s_barrier
	ds_read_b128 v[48:51], v232 offset:32768
	ds_read_b128 v[32:35], v233 offset:32768
	ds_read_b128 v[52:55], v234 offset:32768
	ds_read_b128 v[36:39], v235 offset:32768
	ds_read_b128 v[56:59], v236 offset:32768
	ds_read_b128 v[40:43], v237 offset:32768
	ds_read_b128 v[60:63], v238 offset:32768
	ds_read_b128 v[44:47], v239 offset:32768
	s_waitcnt lgkmcnt(0)
	s_mov_b64 s[52:53], 0x200
	v_lshl_add_u64 v[224:225], v[164:165], 0, s[52:53]
	v_lshl_add_u64 v[224:225], v[224:225], 0, s[62:63]
	s_add_i32 s54, s36, 0x0
	s_add_i32 m0, s54, s64
	s_nop 0
	global_load_lds_dwordx4 v[224:225], off nt
	s_mov_b64 s[52:53], 0x4200
	v_lshl_add_u64 v[224:225], v[24:25], 0, s[52:53]
	v_lshl_add_u64 v[224:225], v[224:225], 0, s[62:63]
	s_add_i32 s54, s36, 0x400
	s_add_i32 m0, s54, s64
	s_nop 0
	global_load_lds_dwordx4 v[224:225], off nt
	s_mov_b64 s[52:53], 0x8200
	v_lshl_add_u64 v[224:225], v[26:27], 0, s[52:53]
	v_lshl_add_u64 v[224:225], v[224:225], 0, s[62:63]
	s_add_i32 s54, s36, 0x800
	s_add_i32 m0, s54, s64
	s_nop 0
	global_load_lds_dwordx4 v[224:225], off nt
	s_mov_b64 s[52:53], 0xc200
	v_lshl_add_u64 v[224:225], v[28:29], 0, s[52:53]
	v_lshl_add_u64 v[224:225], v[224:225], 0, s[62:63]
	s_add_i32 s54, s36, 0xc00
	s_add_i32 m0, s54, s64
	s_nop 0
	global_load_lds_dwordx4 v[224:225], off nt
	v_lshlrev_b32_e32 v31, 2, v204
	v_max_f32_e32 v80, v65, v65
	v_max_f32_e32 v81, v64, v64
	v_max_f32_e32 v80, v81, v80
	v_max3_f32 v81, v66, v67, v3
	v_max3_f32 v80, v80, v2, v4
	v_max3_f32 v80, v80, v5, v68
	v_max3_f32 v81, v81, v70, v71
	v_max3_f32 v80, v80, v69, v6
	v_max3_f32 v81, v81, v8, v9
	v_max3_f32 v80, v80, v7, v72
	v_max3_f32 v81, v81, v74, v75
	v_max3_f32 v80, v80, v73, v10
	v_max3_f32 v81, v81, v12, v13
	v_max3_f32 v80, v80, v11, v76
	v_max3_f32 v81, v81, v78, v79
	v_max3_f32 v80, v80, v77, v14
	v_max3_f32 v81, v81, v16, v17
	v_max3_f32 v80, v80, v15, v81
	v_mov_b32_e32 v81, v80
	s_nop 1
	v_permlane32_swap_b32_e32 v80, v81
	v_max_f32_e32 v81, v81, v81
	v_max_f32_e32 v80, v80, v80
	v_max_f32_e32 v80, v80, v81
	v_mul_f32_e32 v208, 0x3fb8aa3b, v80
	s_mov_b32 s48, 0
	s_mov_b32 s38, -1
	s_mov_b64 s[0:1], 0x4000
	s_mov_b64 s[8:9], 0x8000
	s_mov_b64 s[24:25], 0xc000
	s_mov_b64 s[14:15], 0x10000
	s_mov_b64 s[26:27], 0x14000
	s_mov_b64 s[28:29], 0x18000
	s_mov_b64 s[30:31], 0x1c000
	v_fma_f32 v64, v64, s39, -v208
	v_fma_f32 v2, v2, s39, -v208
	v_fma_f32 v65, v65, s39, -v208
	v_fma_f32 v3, v3, s39, -v208
	v_fma_f32 v66, v66, s39, -v208
	v_fma_f32 v4, v4, s39, -v208
	v_fma_f32 v67, v67, s39, -v208
	v_fma_f32 v5, v5, s39, -v208
	v_fma_f32 v68, v68, s39, -v208
	v_fma_f32 v6, v6, s39, -v208
	v_fma_f32 v69, v69, s39, -v208
	v_fma_f32 v7, v7, s39, -v208
	v_fma_f32 v70, v70, s39, -v208
	v_fma_f32 v8, v8, s39, -v208
	v_fma_f32 v71, v71, s39, -v208
	v_fma_f32 v9, v9, s39, -v208
	v_fma_f32 v72, v72, s39, -v208
	v_fma_f32 v10, v10, s39, -v208
	v_fma_f32 v73, v73, s39, -v208
	v_fma_f32 v11, v11, s39, -v208
	v_fma_f32 v74, v74, s39, -v208
	v_fma_f32 v12, v12, s39, -v208
	v_fma_f32 v75, v75, s39, -v208
	v_fma_f32 v13, v13, s39, -v208
	v_fma_f32 v76, v76, s39, -v208
	v_fma_f32 v14, v14, s39, -v208
	v_fma_f32 v77, v77, s39, -v208
	v_fma_f32 v78, v78, s39, -v208
	v_fma_f32 v79, v79, s39, -v208
	v_fma_f32 v94, v15, s39, -v208
	v_fma_f32 v16, v16, s39, -v208
	v_fma_f32 v15, v17, s39, -v208
	s_and_b64 vcc, exec, s[4:5]
	s_nop 0
	s_mov_b64 s[42:43], 0x30000
	v_lshl_add_u64 v[22:23], v[22:23], 0, s[42:43]
	s_mov_b32 m0, s37
	s_nop 0
	global_load_lds_dwordx4 v[22:23], off
.LBB3_8:
	v_lshl_add_u64 v[178:179], v[24:25], 0, s[0:1]
	s_and_b32 s0, s40, 0x3fffffc0
	s_lshl_b32 s0, s0, 2
	s_add_i32 s23, s0, 0
	s_add_i32 s0, s7, 0
	s_add_i32 s0, s0, 0x14800
	v_lshlrev_b32_e32 v0, 8, v0
	s_cmp_lg_u32 0, -1
	v_lshl_add_u64 v[174:175], v[28:29], 0, s[24:25]
	v_exp_f32_e32 v80, v64
	v_exp_f32_e32 v64, v2
	v_lshlrev_b32_e32 v2, 10, v106
	v_and_b32_e32 v0, 0x300, v0
	s_cselect_b32 s24, 0, 0
	v_add3_u32 v222, s0, v2, v0
	s_add_i32 s0, s24, s35
	s_add_i32 s24, s24, s7
	v_lshl_add_u64 v[166:167], v[28:29], 0, s[30:31]
	s_add_i32 s0, s0, 0x8000
	s_add_i32 s30, s24, 0x14c00
	s_add_i32 s31, s24, 0x15000
	s_add_i32 s40, s24, 0x15400
	s_add_i32 s41, s24, 0x15800
	s_add_i32 s42, s24, 0x15c00
	s_add_i32 s43, s24, 0x16000
	s_add_i32 s44, s24, 0x16400
	v_lshlrev_b32_e32 v0, 5, v30
	v_lshrrev_b32_e32 v2, 2, v105
	s_add_u32 s20, s6, s20
	v_and_b32_e32 v0, 32, v0
	v_or_b32_e32 v2, v31, v2
	s_addc_u32 s21, 0, s21
	s_lshl_b32 s2, s55, 7
	v_lshl_add_u64 v[176:177], v[26:27], 0, s[8:9]
	v_add_u32_e32 v0, 0, v0
	v_lshlrev_b32_e32 v2, 6, v2
	s_mov_b64 s[8:9], 0x60000
	s_and_b32 s2, s2, 0x780
	v_exp_f32_e32 v81, v65
	v_exp_f32_e32 v65, v3
	v_add3_u32 v207, v0, v104, v2
	v_add_u32_e32 v207, s61, v207
	v_lshl_add_u64 v[2:3], v[162:163], 0, s[8:9]
	s_mov_b32 m0, s0
	s_nop 0
	global_load_lds_dwordx4 v[2:3], off
	v_lshl_add_u64 v[226:227], v[2:3], 0, s[58:59]
	s_add_i32 m0, s0, 0x6800
	s_nop 0
	global_load_lds_dwordx4 v[226:227], off
	v_add_lshl_u32 v184, v202, s3, 10
	v_mov_b32_e32 v185, 0
	s_add_u32 s2, s22, s2
	v_exp_f32_e32 v82, v66
	v_exp_f32_e32 v66, v4
	v_xor_b32_e32 v4, v204, v105
	ds_read_b128 v[112:115], v209 offset:8192
	ds_read_b128 v[104:107], v209 offset:10240
	ds_read_b128 v[116:119], v210 offset:8192
	ds_read_b128 v[108:111], v210 offset:10240
	v_cmp_gt_u32_e64 s[0:1], 32, v1
	v_lshl_add_u64 v[0:1], s[20:21], 0, v[184:185]
	s_addc_u32 s3, 0, 0
	v_lshl_add_u64 v[0:1], v[0:1], 0, v[18:19]
	s_add_u32 s2, s2, s46
	v_lshl_add_u64 v[0:1], s[10:11], 0, v[0:1]
	s_addc_u32 s3, s3, s45
	v_exp_f32_e32 v83, v67
	v_exp_f32_e32 v67, v5
	v_exp_f32_e32 v84, v68
	v_exp_f32_e32 v68, v6
	v_exp_f32_e32 v85, v69
	v_exp_f32_e32 v69, v7
	v_exp_f32_e32 v86, v70
	v_exp_f32_e32 v70, v8
	v_exp_f32_e32 v87, v71
	v_exp_f32_e32 v71, v9
	v_exp_f32_e32 v88, v72
	v_exp_f32_e32 v72, v10
	v_exp_f32_e32 v89, v73
	v_exp_f32_e32 v73, v11
	v_exp_f32_e32 v90, v74
	v_exp_f32_e32 v74, v12
	v_exp_f32_e32 v91, v75
	v_exp_f32_e32 v75, v13
	v_exp_f32_e32 v92, v76
	v_exp_f32_e32 v76, v14
	v_exp_f32_e32 v93, v77
	v_exp_f32_e32 v77, v94
	v_exp_f32_e32 v94, v78
	v_exp_f32_e32 v78, v16
	v_exp_f32_e32 v95, v79
	v_exp_f32_e32 v79, v15
	v_lshl_add_u64 v[180:181], v[0:1], 0, s[14:15]
	v_lshl_add_u64 v[0:1], s[2:3], 0, v[20:21]
	v_mov_b32_e32 v161, v185
	s_waitcnt vmcnt(3) lgkmcnt(0)
	s_barrier
	v_lshlrev_b32_e32 v223, 4, v4
	v_lshl_add_u64 v[0:1], v[0:1], 0, v[160:161]
	v_xor_b32_e32 v2, 0x80, v223
	v_xor_b32_e32 v3, 32, v223
	v_xor_b32_e32 v4, 0xa0, v223
	v_xor_b32_e32 v5, 64, v223
	v_xor_b32_e32 v6, 0xc0, v223
	v_xor_b32_e32 v7, 0x60, v223
	v_xor_b32_e32 v8, 0xe0, v223
	v_lshl_add_u64 v[0:1], s[12:13], 0, v[0:1]
	v_lshl_add_u64 v[172:173], v[164:165], 0, s[14:15]
	v_lshl_add_u64 v[170:171], v[24:25], 0, s[26:27]
	v_lshl_add_u64 v[168:169], v[26:27], 0, s[28:29]
	v_lshl_add_u32 v206, v203, 2, s23
	v_lshl_add_u32 v205, v31, 2, s23
	v_lshl_add_u64 v[182:183], v[0:1], 0, s[8:9]
	s_movk_i32 s45, 0x4000
	s_movk_i32 s47, 0x2000
	s_mov_b64 s[2:3], 0
	s_mov_b32 s46, 0x41000000
	s_mov_b64 s[10:11], 0x30000
	s_mov_b64 s[12:13], 0x300
	s_mov_b64 s[14:15], 0x40000
	s_mov_b64 s[20:21], 0xc0000
	s_mov_b64 s[22:23], 0x400
	s_mov_b64 s[24:25], 0x20000
	v_add_u32_e32 v161, v222, v2
	v_add_u32_e32 v184, v222, v3
	v_add_u32_e32 v211, v222, v4
	v_add_u32_e32 v212, v222, v5
	v_add_u32_e32 v213, v222, v6
	v_add_u32_e32 v214, v222, v7
	v_add_u32_e32 v215, v222, v8
	v_mov_b32_e32 v0, v185
	v_mov_b32_e32 v1, v185
	v_mov_b32_e32 v2, v185
	v_mov_b32_e32 v3, v185
	v_mov_b32_e32 v4, v185
	v_mov_b32_e32 v5, v185
	v_mov_b32_e32 v6, v185
	v_mov_b32_e32 v7, v185
	v_mov_b32_e32 v8, v185
	v_mov_b32_e32 v9, v185
	v_mov_b32_e32 v10, v185
	v_mov_b32_e32 v11, v185
	v_mov_b32_e32 v12, v185
	v_mov_b32_e32 v13, v185
	v_mov_b32_e32 v14, v185
	v_mov_b32_e32 v15, v185
	v_mov_b32_e32 v16, v185
	v_mov_b32_e32 v17, v185
	v_mov_b32_e32 v18, v185
	v_mov_b32_e32 v19, v185
	v_mov_b32_e32 v20, v185
	v_mov_b32_e32 v21, v185
	v_mov_b32_e32 v22, v185
	v_mov_b32_e32 v23, v185
	v_mov_b32_e32 v24, v185
	v_mov_b32_e32 v25, v185
	v_mov_b32_e32 v26, v185
	v_mov_b32_e32 v27, v185
	v_mov_b32_e32 v28, v185
	v_mov_b32_e32 v29, v185
	v_mov_b32_e32 v30, v185
	v_mov_b32_e32 v31, v185
	v_add_u32_e32 v221, v222, v223
.LBB3_9:
	v_add_u32_e32 v138, s48, v207
	ds_read_b64_tr_b16 v[156:157], v138 offset:24576
	ds_read_b64_tr_b16 v[158:159], v138 offset:25088
	v_add_f32_e32 v120, v80, v81
	s_waitcnt lgkmcnt(3)
	v_mfma_scale_f32_32x32x64_f8f6f4 v[48:63], v[112:119], v[96:103], v[48:63], v219, v220 op_sel_hi:[0,0,0]
	v_add_f32_e32 v112, v82, v120
	v_add_f32_e32 v112, v83, v112
	v_add_f32_e32 v112, v84, v112
	v_add_f32_e32 v116, v85, v112
	v_cvt_pk_f16_f32 v132, v80, v81
	v_cvt_pk_f16_f32 v133, v82, v83
	ds_read_b64_tr_b16 v[112:113], v138 offset:28672
	ds_read_b64_tr_b16 v[114:115], v138 offset:29184
	v_add_f32_e32 v80, v86, v116
	v_add_f32_e32 v80, v87, v80
	v_add_f32_e32 v80, v88, v80
	v_add_f32_e32 v80, v89, v80
	v_cvt_pk_f16_f32 v134, v84, v85
	v_cvt_pk_f16_f32 v135, v86, v87
	s_waitcnt lgkmcnt(4)
	v_mfma_scale_f32_32x32x64_f8f6f4 v[32:47], v[104:111], v[96:103], v[32:47], v219, v220 op_sel_hi:[0,0,0]
	v_lshl_add_u64 v[186:187], v[164:165], 0, s[2:3]
	v_lshl_add_u64 v[228:229], v[186:187], 0, s[12:13]
	v_lshl_add_u64 v[228:229], v[228:229], 0, s[62:63]
	s_add_i32 m0, s36, s65
	s_nop 0
	global_load_lds_dwordx4 v[228:229], off nt
	ds_read_b64_tr_b16 v[104:105], v138 offset:25600
	ds_read_b64_tr_b16 v[106:107], v138 offset:26112
	v_lshl_add_u64 v[188:189], v[178:179], 0, s[2:3]
	v_lshl_add_u64 v[228:229], v[188:189], 0, s[12:13]
	v_lshl_add_u64 v[228:229], v[228:229], 0, s[62:63]
	s_add_i32 m0, s30, s65
	s_nop 0
	global_load_lds_dwordx4 v[228:229], off nt
	v_add_f32_e32 v80, v90, v80
	v_add_f32_e32 v80, v91, v80
	v_add_f32_e32 v80, v92, v80
	v_add_f32_e32 v80, v93, v80
	v_cvt_pk_f16_f32 v128, v88, v89
	v_cvt_pk_f16_f32 v129, v90, v91
	ds_read_b64_tr_b16 v[152:153], v138 offset:29696
	ds_read_b64_tr_b16 v[154:155], v138 offset:30208
	v_lshl_add_u64 v[190:191], v[176:177], 0, s[2:3]
	v_lshl_add_u64 v[228:229], v[190:191], 0, s[12:13]
	v_lshl_add_u64 v[228:229], v[228:229], 0, s[62:63]
	s_add_i32 m0, s31, s65
	s_nop 0
	global_load_lds_dwordx4 v[228:229], off nt
	v_add_f32_e32 v80, v94, v80
	v_add_f32_e32 v80, v95, v80
	v_add_f32_e32 v80, v64, v80
	v_add_f32_e32 v80, v65, v80
	v_cvt_pk_f16_f32 v130, v92, v93
	v_cvt_pk_f16_f32 v131, v94, v95
	ds_read_b64_tr_b16 v[148:149], v138 offset:26624
	ds_read_b64_tr_b16 v[150:151], v138 offset:27136
	v_lshl_add_u64 v[192:193], v[174:175], 0, s[2:3]
	v_lshl_add_u64 v[228:229], v[192:193], 0, s[12:13]
	v_lshl_add_u64 v[228:229], v[228:229], 0, s[62:63]
	s_add_i32 m0, s40, s65
	s_nop 0
	global_load_lds_dwordx4 v[228:229], off nt
	v_add_f32_e32 v80, v66, v80
	v_add_f32_e32 v80, v67, v80
	v_add_f32_e32 v80, v68, v80
	v_add_f32_e32 v80, v69, v80
	v_cvt_pk_f16_f32 v124, v64, v65
	v_cvt_pk_f16_f32 v125, v66, v67
	ds_read_b64_tr_b16 v[144:145], v138 offset:30720
	ds_read_b64_tr_b16 v[146:147], v138 offset:31232
	v_add_f32_e32 v64, v70, v80
	v_add_f32_e32 v64, v71, v64
	v_add_f32_e32 v64, v72, v64
	v_add_f32_e32 v64, v73, v64
	v_cvt_pk_f16_f32 v126, v68, v69
	v_cvt_pk_f16_f32 v127, v70, v71
	ds_read_b64_tr_b16 v[140:141], v138 offset:27648
	ds_read_b64_tr_b16 v[142:143], v138 offset:28160
	v_add_f32_e32 v64, v74, v64
	v_add_f32_e32 v64, v75, v64
	v_add_f32_e32 v64, v76, v64
	v_add_f32_e32 v64, v77, v64
	v_cvt_pk_f16_f32 v120, v72, v73
	v_cvt_pk_f16_f32 v121, v74, v75
	ds_read_b64_tr_b16 v[136:137], v138 offset:31744
	ds_read_b64_tr_b16 v[138:139], v138 offset:32256
	v_add_f32_e32 v64, v78, v64
	v_add_f32_e32 v64, v79, v64
	v_add_f32_e32 v108, 0, v64
	v_cvt_pk_f16_f32 v122, v76, v77
	v_cvt_pk_f16_f32 v123, v78, v79
	s_nop 1
	s_nop 0
	v_add_f32_e32 v185, v185, v108
	v_max_f32_e32 v108, v49, v49
	v_max_f32_e32 v109, v48, v48
	v_max_f32_e32 v108, v109, v108
	v_max3_f32 v109, v50, v51, v33
	v_max3_f32 v108, v108, v32, v34
	v_max3_f32 v108, v108, v35, v52
	v_max3_f32 v109, v109, v54, v55
	v_max3_f32 v108, v108, v53, v36
	v_max3_f32 v109, v109, v38, v39
	v_max3_f32 v108, v108, v37, v56
	v_max3_f32 v109, v109, v58, v59
	v_add_u32_e32 v221, v222, v223
	v_max3_f32 v108, v108, v57, v40
	v_max3_f32 v109, v109, v42, v43
	ds_read_b128 v[80:83], v221
	ds_read_b128 v[64:67], v161
	ds_read_b128 v[84:87], v184
	ds_read_b128 v[68:71], v211
	ds_read_b128 v[88:91], v212
	ds_read_b128 v[72:75], v213
	ds_read_b128 v[92:95], v214
	ds_read_b128 v[76:79], v215
	v_max3_f32 v108, v108, v41, v60
	v_max3_f32 v109, v109, v62, v63
	v_max3_f32 v108, v108, v61, v44
	v_max3_f32 v109, v109, v46, v47
	v_max3_f32 v108, v108, v45, v109
	v_mov_b32_e32 v109, v108
	s_nop 1
	v_permlane32_swap_b32_e32 v108, v109
	v_max_f32_e32 v109, v109, v109
	v_max_f32_e32 v108, v108, v108
	v_max_f32_e32 v108, v108, v109
	v_fma_f32 v108, v108, s39, -v208
	v_cmp_lt_f32_e32 vcc, s46, v108
	s_cmp_lg_u64 vcc, 0
	s_cselect_b64 s[26:27], -1, 0
	s_cbranch_vccnz .LBB3_21
.LBB3_10:
	s_waitcnt lgkmcnt(14)
	v_mfma_f32_32x32x16_f16 v[0:15], v[132:135], v[156:159], v[0:15]
	v_fma_f32 v48, v48, s39, -v208
	v_fma_f32 v49, v49, s39, -v208
	v_fma_f32 v50, v50, s39, -v208
	v_fma_f32 v51, v51, s39, -v208
	v_exp_f32_e32 v48, v48
	v_exp_f32_e32 v49, v49
	v_exp_f32_e32 v50, v50
	v_exp_f32_e32 v51, v51
	s_and_b64 vcc, exec, s[4:5]
	s_nop 0
	v_lshl_add_u64 v[108:109], v[180:181], 0, s[10:11]
	s_add_i32 s28, s47, s37
	s_mov_b32 m0, s28
	s_nop 0
	global_load_lds_dwordx4 v[108:109], off
.LBB3_12:
	v_mfma_f32_32x32x16_f16 v[16:31], v[132:135], v[112:115], v[16:31]
	v_fma_f32 v52, v52, s39, -v208
	v_fma_f32 v53, v53, s39, -v208
	v_fma_f32 v54, v54, s39, -v208
	v_fma_f32 v55, v55, s39, -v208
	v_exp_f32_e32 v52, v52
	v_exp_f32_e32 v53, v53
	v_exp_f32_e32 v54, v54
	v_exp_f32_e32 v55, v55
	v_lshl_add_u64 v[108:109], v[182:183], 0, s[8:9]
	s_add_i32 s28, s45, s34
	s_mov_b32 m0, s28
	s_nop 0
	global_load_lds_dwordx4 v[108:109], off
	v_lshl_add_u64 v[226:227], v[108:109], 0, s[58:59]
	s_add_i32 m0, s28, 0x6800
	s_nop 0
	global_load_lds_dwordx4 v[226:227], off
	s_waitcnt lgkmcnt(0)
	v_add_u32_e32 v108, s45, v216
	v_add_u32_e32 v109, v108, v217
	v_add_u32_e32 v108, v108, v218
	ds_read_b128 v[112:115], v109
	ds_read_b128 v[116:119], v108
	v_mfma_f32_32x32x16_f16 v[0:15], v[128:131], v[104:107], v[0:15]
	v_fma_f32 v56, v56, s39, -v208
	v_fma_f32 v57, v57, s39, -v208
	v_fma_f32 v58, v58, s39, -v208
	v_fma_f32 v59, v59, s39, -v208
	v_exp_f32_e32 v56, v56
	v_exp_f32_e32 v57, v57
	v_exp_f32_e32 v58, v58
	v_exp_f32_e32 v59, v59
	ds_read_b128 v[104:107], v109 offset:2048
	ds_read_b128 v[108:111], v108 offset:2048
	v_mfma_f32_32x32x16_f16 v[16:31], v[128:131], v[152:155], v[16:31]
	v_fma_f32 v60, v60, s39, -v208
	v_fma_f32 v61, v61, s39, -v208
	v_fma_f32 v62, v62, s39, -v208
	v_fma_f32 v63, v63, s39, -v208
	v_exp_f32_e32 v60, v60
	v_exp_f32_e32 v61, v61
	v_exp_f32_e32 v62, v62
	v_exp_f32_e32 v63, v63
	v_mfma_f32_32x32x16_f16 v[0:15], v[124:127], v[148:151], v[0:15]
	v_fma_f32 v32, v32, s39, -v208
	v_fma_f32 v33, v33, s39, -v208
	v_fma_f32 v34, v34, s39, -v208
	v_fma_f32 v35, v35, s39, -v208
	v_exp_f32_e32 v32, v32
	v_exp_f32_e32 v33, v33
	v_exp_f32_e32 v34, v34
	v_exp_f32_e32 v35, v35
	s_waitcnt lgkmcnt(14)
	v_mfma_f32_32x32x16_f16 v[16:31], v[124:127], v[144:147], v[16:31]
	v_fma_f32 v36, v36, s39, -v208
	v_fma_f32 v37, v37, s39, -v208
	v_fma_f32 v38, v38, s39, -v208
	v_fma_f32 v39, v39, s39, -v208
	v_exp_f32_e32 v36, v36
	v_exp_f32_e32 v37, v37
	v_exp_f32_e32 v38, v38
	v_exp_f32_e32 v39, v39
	v_lshl_add_u64 v[194:195], v[172:173], 0, s[2:3]
	v_mfma_f32_32x32x16_f16 v[0:15], v[120:123], v[140:143], v[0:15]
	v_fma_f32 v40, v40, s39, -v208
	v_fma_f32 v41, v41, s39, -v208
	v_fma_f32 v42, v42, s39, -v208
	v_fma_f32 v43, v43, s39, -v208
	v_exp_f32_e32 v40, v40
	v_exp_f32_e32 v41, v41
	v_exp_f32_e32 v42, v42
	v_exp_f32_e32 v43, v43
	v_lshl_add_u64 v[196:197], v[170:171], 0, s[2:3]
	s_waitcnt lgkmcnt(12)
	v_mfma_f32_32x32x16_f16 v[16:31], v[120:123], v[136:139], v[16:31]
	v_fma_f32 v44, v44, s39, -v208
	v_fma_f32 v45, v45, s39, -v208
	v_fma_f32 v46, v46, s39, -v208
	v_fma_f32 v47, v47, s39, -v208
	v_exp_f32_e32 v44, v44
	v_exp_f32_e32 v45, v45
	v_exp_f32_e32 v46, v46
	v_exp_f32_e32 v47, v47
	v_lshl_add_u64 v[198:199], v[168:169], 0, s[2:3]
	v_lshl_add_u64 v[200:201], v[166:167], 0, s[2:3]
	s_waitcnt vmcnt(3) lgkmcnt(0)
	s_barrier
	s_andn2_b64 vcc, exec, s[26:27]
	s_cbranch_vccnz .LBB3_14
	ds_read_b128 v[136:139], v205 offset:49248
	ds_read_b128 v[140:143], v205 offset:49216
	ds_read_b128 v[144:147], v205 offset:49184
	ds_read_b128 v[148:151], v205 offset:49152
	s_waitcnt lgkmcnt(3)
	v_pk_mul_f32 v[14:15], v[14:15], v[138:139]
	s_waitcnt lgkmcnt(2)
	v_pk_mul_f32 v[10:11], v[10:11], v[142:143]
	s_waitcnt lgkmcnt(1)
	v_pk_mul_f32 v[6:7], v[6:7], v[146:147]
	s_waitcnt lgkmcnt(0)
	v_pk_mul_f32 v[2:3], v[2:3], v[150:151]
	v_pk_mul_f32 v[12:13], v[12:13], v[136:137]
	v_pk_mul_f32 v[8:9], v[8:9], v[140:141]
	v_pk_mul_f32 v[4:5], v[4:5], v[144:145]
	v_pk_mul_f32 v[0:1], v[0:1], v[148:149]
	v_pk_mul_f32 v[30:31], v[30:31], v[138:139]
	v_pk_mul_f32 v[26:27], v[26:27], v[142:143]
	v_pk_mul_f32 v[22:23], v[22:23], v[146:147]
	v_pk_mul_f32 v[18:19], v[18:19], v[150:151]
	v_pk_mul_f32 v[28:29], v[28:29], v[136:137]
	v_pk_mul_f32 v[24:25], v[24:25], v[140:141]
	v_pk_mul_f32 v[20:21], v[20:21], v[144:145]
	v_pk_mul_f32 v[16:17], v[16:17], v[148:149]
.LBB3_14:
	v_add_u32_e32 v138, s47, v207
	ds_read_b64_tr_b16 v[156:157], v138 offset:24576
	ds_read_b64_tr_b16 v[158:159], v138 offset:25088
	v_add_f32_e32 v120, v48, v49
	s_waitcnt lgkmcnt(4)
	v_mfma_scale_f32_32x32x64_f8f6f4 v[80:95], v[112:119], v[96:103], v[80:95], v219, v220 op_sel_hi:[0,0,0]
	v_add_f32_e32 v112, v50, v120
	v_add_f32_e32 v112, v51, v112
	v_add_f32_e32 v112, v52, v112
	v_add_f32_e32 v116, v53, v112
	v_cvt_pk_f16_f32 v132, v48, v49
	v_cvt_pk_f16_f32 v133, v50, v51
	ds_read_b64_tr_b16 v[112:113], v138 offset:28672
	ds_read_b64_tr_b16 v[114:115], v138 offset:29184
	v_add_f32_e32 v48, v54, v116
	v_add_f32_e32 v48, v55, v48
	v_add_f32_e32 v48, v56, v48
	v_add_f32_e32 v48, v57, v48
	v_cvt_pk_f16_f32 v134, v52, v53
	v_cvt_pk_f16_f32 v135, v54, v55
	s_waitcnt lgkmcnt(4)
	v_mfma_scale_f32_32x32x64_f8f6f4 v[64:79], v[104:111], v[96:103], v[64:79], v219, v220 op_sel_hi:[0,0,0]
	v_lshl_add_u64 v[228:229], v[186:187], 0, s[22:23]
	v_lshl_add_u64 v[228:229], v[228:229], 0, s[62:63]
	s_add_i32 m0, s36, s64
	s_nop 0
	global_load_lds_dwordx4 v[228:229], off nt
	ds_read_b64_tr_b16 v[104:105], v138 offset:25600
	ds_read_b64_tr_b16 v[106:107], v138 offset:26112
	v_lshl_add_u64 v[228:229], v[188:189], 0, s[22:23]
	v_lshl_add_u64 v[228:229], v[228:229], 0, s[62:63]
	s_add_i32 m0, s30, s64
	s_nop 0
	global_load_lds_dwordx4 v[228:229], off nt
	v_add_f32_e32 v48, v58, v48
	v_add_f32_e32 v48, v59, v48
	v_add_f32_e32 v48, v60, v48
	v_add_f32_e32 v48, v61, v48
	v_cvt_pk_f16_f32 v128, v56, v57
	v_cvt_pk_f16_f32 v129, v58, v59
	ds_read_b64_tr_b16 v[152:153], v138 offset:29696
	ds_read_b64_tr_b16 v[154:155], v138 offset:30208
	v_lshl_add_u64 v[228:229], v[190:191], 0, s[22:23]
	v_lshl_add_u64 v[228:229], v[228:229], 0, s[62:63]
	s_add_i32 m0, s31, s64
	s_nop 0
	global_load_lds_dwordx4 v[228:229], off nt
	v_add_f32_e32 v48, v62, v48
	v_add_f32_e32 v48, v63, v48
	v_add_f32_e32 v48, v32, v48
	v_add_f32_e32 v48, v33, v48
	v_cvt_pk_f16_f32 v130, v60, v61
	v_cvt_pk_f16_f32 v131, v62, v63
	ds_read_b64_tr_b16 v[148:149], v138 offset:26624
	ds_read_b64_tr_b16 v[150:151], v138 offset:27136
	v_lshl_add_u64 v[228:229], v[192:193], 0, s[22:23]
	v_lshl_add_u64 v[228:229], v[228:229], 0, s[62:63]
	s_add_i32 m0, s40, s64
	s_nop 0
	global_load_lds_dwordx4 v[228:229], off nt
	v_add_f32_e32 v48, v34, v48
	v_add_f32_e32 v48, v35, v48
	v_add_f32_e32 v48, v36, v48
	v_add_f32_e32 v48, v37, v48
	v_cvt_pk_f16_f32 v124, v32, v33
	v_cvt_pk_f16_f32 v125, v34, v35
	ds_read_b64_tr_b16 v[144:145], v138 offset:30720
	ds_read_b64_tr_b16 v[146:147], v138 offset:31232
	v_add_f32_e32 v32, v38, v48
	v_add_f32_e32 v32, v39, v32
	v_add_f32_e32 v32, v40, v32
	v_add_f32_e32 v32, v41, v32
	v_cvt_pk_f16_f32 v126, v36, v37
	v_cvt_pk_f16_f32 v127, v38, v39
	ds_read_b64_tr_b16 v[140:141], v138 offset:27648
	ds_read_b64_tr_b16 v[142:143], v138 offset:28160
	v_add_f32_e32 v32, v42, v32
	v_add_f32_e32 v32, v43, v32
	v_add_f32_e32 v32, v44, v32
	v_add_f32_e32 v32, v45, v32
	v_cvt_pk_f16_f32 v120, v40, v41
	v_cvt_pk_f16_f32 v121, v42, v43
	ds_read_b64_tr_b16 v[136:137], v138 offset:31744
	ds_read_b64_tr_b16 v[138:139], v138 offset:32256
	v_add_f32_e32 v32, v46, v32
	v_add_f32_e32 v32, v47, v32
	v_add_f32_e32 v108, 0, v32
	v_cvt_pk_f16_f32 v122, v44, v45
	v_cvt_pk_f16_f32 v123, v46, v47
	s_nop 1
	s_nop 0
	v_add_f32_e32 v185, v185, v108
	v_max_f32_e32 v108, v81, v81
	v_max_f32_e32 v109, v80, v80
	v_max_f32_e32 v108, v109, v108
	v_max3_f32 v109, v82, v83, v65
	v_max3_f32 v108, v108, v64, v66
	v_max3_f32 v108, v108, v67, v84
	v_max3_f32 v109, v109, v86, v87
	v_max3_f32 v108, v108, v85, v68
	v_max3_f32 v109, v109, v70, v71
	v_max3_f32 v108, v108, v69, v88
	v_max3_f32 v109, v109, v90, v91
	v_max3_f32 v108, v108, v89, v72
	v_max3_f32 v109, v109, v74, v75
	ds_read_b128 v[48:51], v221 offset:32768
	ds_read_b128 v[32:35], v161 offset:32768
	ds_read_b128 v[52:55], v184 offset:32768
	ds_read_b128 v[36:39], v211 offset:32768
	ds_read_b128 v[56:59], v212 offset:32768
	ds_read_b128 v[40:43], v213 offset:32768
	ds_read_b128 v[60:63], v214 offset:32768
	ds_read_b128 v[44:47], v215 offset:32768
	v_max3_f32 v108, v108, v73, v92
	v_max3_f32 v109, v109, v94, v95
	v_max3_f32 v108, v108, v93, v76
	v_max3_f32 v109, v109, v78, v79
	v_max3_f32 v108, v108, v77, v109
	v_mov_b32_e32 v109, v108
	s_nop 1
	v_permlane32_swap_b32_e32 v108, v109
	v_max_f32_e32 v109, v109, v109
	v_max_f32_e32 v108, v108, v108
	v_max_f32_e32 v108, v108, v109
	v_fma_f32 v108, v108, s39, -v208
	v_cmp_lt_f32_e32 vcc, s46, v108
	s_cmp_lg_u64 vcc, 0
	s_cselect_b64 s[26:27], -1, 0
	s_cbranch_vccnz .LBB3_24
.LBB3_15:
	s_waitcnt lgkmcnt(14)
	v_mfma_f32_32x32x16_f16 v[0:15], v[132:135], v[156:159], v[0:15]
	v_fma_f32 v80, v80, s39, -v208
	v_fma_f32 v81, v81, s39, -v208
	v_fma_f32 v82, v82, s39, -v208
	v_fma_f32 v83, v83, s39, -v208
	v_exp_f32_e32 v80, v80
	v_exp_f32_e32 v81, v81
	v_exp_f32_e32 v82, v82
	v_exp_f32_e32 v83, v83
	s_and_b64 vcc, exec, s[4:5]
	s_nop 0
	v_lshl_add_u64 v[108:109], v[180:181], 0, s[14:15]
	s_add_i32 s28, s45, s37
	s_mov_b32 m0, s28
	s_nop 0
	global_load_lds_dwordx4 v[108:109], off
.LBB3_17:
	s_add_i32 s28, s45, 0x2000
	s_cmpk_lg_i32 s45, 0x4000
	s_cselect_b32 s47, s28, 0
	v_mfma_f32_32x32x16_f16 v[16:31], v[132:135], v[112:115], v[16:31]
	v_fma_f32 v84, v84, s39, -v208
	v_fma_f32 v85, v85, s39, -v208
	v_fma_f32 v86, v86, s39, -v208
	v_fma_f32 v87, v87, s39, -v208
	v_exp_f32_e32 v84, v84
	v_exp_f32_e32 v85, v85
	v_exp_f32_e32 v86, v86
	v_exp_f32_e32 v87, v87
	v_lshl_add_u64 v[182:183], v[182:183], 0, s[20:21]
	s_add_i32 s28, s47, s34
	s_mov_b32 m0, s28
	s_nop 0
	global_load_lds_dwordx4 v[182:183], off
	v_lshl_add_u64 v[226:227], v[182:183], 0, s[58:59]
	s_add_i32 m0, s28, 0x6800
	s_nop 0
	global_load_lds_dwordx4 v[226:227], off
	s_waitcnt lgkmcnt(0)
	v_add_u32_e32 v108, s47, v216
	v_add_u32_e32 v109, v108, v217
	v_add_u32_e32 v108, v108, v218
	ds_read_b128 v[112:115], v109
	ds_read_b128 v[116:119], v108
	v_mfma_f32_32x32x16_f16 v[0:15], v[128:131], v[104:107], v[0:15]
	v_fma_f32 v88, v88, s39, -v208
	v_fma_f32 v89, v89, s39, -v208
	v_fma_f32 v90, v90, s39, -v208
	v_fma_f32 v91, v91, s39, -v208
	v_exp_f32_e32 v88, v88
	v_exp_f32_e32 v89, v89
	v_exp_f32_e32 v90, v90
	v_exp_f32_e32 v91, v91
	ds_read_b128 v[104:107], v109 offset:2048
	ds_read_b128 v[108:111], v108 offset:2048
	v_mfma_f32_32x32x16_f16 v[16:31], v[128:131], v[152:155], v[16:31]
	v_fma_f32 v92, v92, s39, -v208
	v_fma_f32 v93, v93, s39, -v208
	v_fma_f32 v94, v94, s39, -v208
	v_fma_f32 v95, v95, s39, -v208
	v_exp_f32_e32 v92, v92
	v_exp_f32_e32 v93, v93
	v_exp_f32_e32 v94, v94
	v_exp_f32_e32 v95, v95
	v_mfma_f32_32x32x16_f16 v[0:15], v[124:127], v[148:151], v[0:15]
	v_fma_f32 v64, v64, s39, -v208
	v_fma_f32 v65, v65, s39, -v208
	v_fma_f32 v66, v66, s39, -v208
	v_fma_f32 v67, v67, s39, -v208
	v_exp_f32_e32 v64, v64
	v_exp_f32_e32 v65, v65
	v_exp_f32_e32 v66, v66
	v_exp_f32_e32 v67, v67
	s_waitcnt lgkmcnt(14)
	v_mfma_f32_32x32x16_f16 v[16:31], v[124:127], v[144:147], v[16:31]
	v_fma_f32 v68, v68, s39, -v208
	v_fma_f32 v69, v69, s39, -v208
	v_fma_f32 v70, v70, s39, -v208
	v_fma_f32 v71, v71, s39, -v208
	v_exp_f32_e32 v68, v68
	v_exp_f32_e32 v69, v69
	v_exp_f32_e32 v70, v70
	v_exp_f32_e32 v71, v71
	v_mfma_f32_32x32x16_f16 v[0:15], v[120:123], v[140:143], v[0:15]
	v_fma_f32 v72, v72, s39, -v208
	v_fma_f32 v73, v73, s39, -v208
	v_fma_f32 v74, v74, s39, -v208
	v_fma_f32 v75, v75, s39, -v208
	v_exp_f32_e32 v72, v72
	v_exp_f32_e32 v73, v73
	v_exp_f32_e32 v74, v74
	v_exp_f32_e32 v75, v75
	s_waitcnt lgkmcnt(12)
	v_mfma_f32_32x32x16_f16 v[16:31], v[120:123], v[136:139], v[16:31]
	v_fma_f32 v76, v76, s39, -v208
	v_fma_f32 v77, v77, s39, -v208
	v_fma_f32 v78, v78, s39, -v208
	v_fma_f32 v79, v79, s39, -v208
	v_exp_f32_e32 v76, v76
	v_exp_f32_e32 v77, v77
	v_exp_f32_e32 v78, v78
	v_exp_f32_e32 v79, v79
	s_waitcnt vmcnt(3) lgkmcnt(0)
	s_barrier
	s_andn2_b64 vcc, exec, s[26:27]
	s_cbranch_vccnz .LBB3_19
	ds_read_b128 v[136:139], v205 offset:49248
	ds_read_b128 v[140:143], v205 offset:49216
	ds_read_b128 v[144:147], v205 offset:49184
	ds_read_b128 v[148:151], v205 offset:49152
	s_waitcnt lgkmcnt(3)
	v_pk_mul_f32 v[14:15], v[14:15], v[138:139]
	s_waitcnt lgkmcnt(2)
	v_pk_mul_f32 v[10:11], v[10:11], v[142:143]
	s_waitcnt lgkmcnt(1)
	v_pk_mul_f32 v[6:7], v[6:7], v[146:147]
	s_waitcnt lgkmcnt(0)
	v_pk_mul_f32 v[2:3], v[2:3], v[150:151]
	v_pk_mul_f32 v[12:13], v[12:13], v[136:137]
	v_pk_mul_f32 v[8:9], v[8:9], v[140:141]
	v_pk_mul_f32 v[4:5], v[4:5], v[144:145]
	v_pk_mul_f32 v[0:1], v[0:1], v[148:149]
	v_pk_mul_f32 v[30:31], v[30:31], v[138:139]
	v_pk_mul_f32 v[26:27], v[26:27], v[142:143]
	v_pk_mul_f32 v[22:23], v[22:23], v[146:147]
	v_pk_mul_f32 v[18:19], v[18:19], v[150:151]
	v_pk_mul_f32 v[28:29], v[28:29], v[136:137]
	v_pk_mul_f32 v[24:25], v[24:25], v[140:141]
	v_pk_mul_f32 v[20:21], v[20:21], v[144:145]
	v_pk_mul_f32 v[16:17], v[16:17], v[148:149]

.LBB3_27:
	ds_read_b64_tr_b16 v[156:157], v207 offset:24576
	ds_read_b64_tr_b16 v[158:159], v207 offset:25088
	v_add_f32_e32 v120, v80, v81
	v_mov_b32_e32 v121, 0x7f7f7f7f
	v_mov_b32_e32 v124, 0x7c7c7c7c
	s_waitcnt lgkmcnt(4)
	v_mfma_scale_f32_32x32x64_f8f6f4 v[48:63], v[112:119], v[96:103], v[48:63], v121, v124 op_sel_hi:[0,0,0]
	v_add_f32_e32 v112, v82, v120
	v_add_f32_e32 v112, v83, v112
	v_add_f32_e32 v112, v84, v112
	v_add_f32_e32 v116, v85, v112
	v_cvt_pk_f16_f32 v132, v80, v81
	v_cvt_pk_f16_f32 v133, v82, v83
	ds_read_b64_tr_b16 v[112:113], v207 offset:28672
	ds_read_b64_tr_b16 v[114:115], v207 offset:29184
	v_add_f32_e32 v80, v86, v116
	v_add_f32_e32 v80, v87, v80
	v_add_f32_e32 v80, v88, v80
	v_add_f32_e32 v80, v89, v80
	v_cvt_pk_f16_f32 v134, v84, v85
	v_cvt_pk_f16_f32 v135, v86, v87
	s_waitcnt lgkmcnt(4)
	v_mfma_scale_f32_32x32x64_f8f6f4 v[32:47], v[104:111], v[96:103], v[32:47], v121, v124 op_sel_hi:[0,0,0]
	ds_read_b64_tr_b16 v[104:105], v207 offset:25600
	ds_read_b64_tr_b16 v[106:107], v207 offset:26112
	v_add_f32_e32 v80, v90, v80
	v_add_f32_e32 v80, v91, v80
	v_add_f32_e32 v80, v92, v80
	v_add_f32_e32 v80, v93, v80
	v_cvt_pk_f16_f32 v128, v88, v89
	v_cvt_pk_f16_f32 v129, v90, v91
	ds_read_b64_tr_b16 v[152:153], v207 offset:29696
	ds_read_b64_tr_b16 v[154:155], v207 offset:30208
	v_add_f32_e32 v80, v94, v80
	v_add_f32_e32 v80, v95, v80
	v_add_f32_e32 v80, v64, v80
	v_add_f32_e32 v80, v65, v80
	v_cvt_pk_f16_f32 v130, v92, v93
	v_cvt_pk_f16_f32 v131, v94, v95
	ds_read_b64_tr_b16 v[148:149], v207 offset:26624
	ds_read_b64_tr_b16 v[150:151], v207 offset:27136
	v_add_f32_e32 v80, v66, v80
	v_add_f32_e32 v80, v67, v80
	v_add_f32_e32 v80, v68, v80
	v_add_f32_e32 v80, v69, v80
	v_cvt_pk_f16_f32 v124, v64, v65
	v_cvt_pk_f16_f32 v125, v66, v67
	ds_read_b64_tr_b16 v[144:145], v207 offset:30720
	ds_read_b64_tr_b16 v[146:147], v207 offset:31232
	v_add_f32_e32 v64, v70, v80
	v_add_f32_e32 v64, v71, v64
	v_add_f32_e32 v64, v72, v64
	v_add_f32_e32 v64, v73, v64
	v_cvt_pk_f16_f32 v126, v68, v69
	v_cvt_pk_f16_f32 v127, v70, v71
	ds_read_b64_tr_b16 v[140:141], v207 offset:27648
	ds_read_b64_tr_b16 v[142:143], v207 offset:28160
	v_add_f32_e32 v64, v74, v64
	v_add_f32_e32 v64, v75, v64
	v_add_f32_e32 v64, v76, v64
	v_add_f32_e32 v64, v77, v64
	v_cvt_pk_f16_f32 v120, v72, v73
	v_cvt_pk_f16_f32 v121, v74, v75
	ds_read_b64_tr_b16 v[136:137], v207 offset:31744
	ds_read_b64_tr_b16 v[138:139], v207 offset:32256
	v_add_f32_e32 v64, v78, v64
	v_add_f32_e32 v64, v79, v64
	v_add_f32_e32 v108, 0, v64
	v_cvt_pk_f16_f32 v122, v76, v77
	v_cvt_pk_f16_f32 v123, v78, v79
	s_nop 1
	s_nop 0
	v_add_f32_e32 v180, v185, v108
	v_max_f32_e32 v108, v49, v49
	v_max_f32_e32 v109, v48, v48
	v_max_f32_e32 v108, v109, v108
	v_max3_f32 v109, v50, v51, v33
	v_max3_f32 v108, v108, v32, v34
	v_max3_f32 v108, v108, v35, v52
	v_max3_f32 v109, v109, v54, v55
	v_max3_f32 v108, v108, v53, v36
	v_max3_f32 v109, v109, v38, v39
	v_max3_f32 v108, v108, v37, v56
	v_max3_f32 v109, v109, v58, v59
	v_max3_f32 v108, v108, v57, v40
	v_max3_f32 v109, v109, v42, v43
	ds_read_b128 v[80:83], v221
	ds_read_b128 v[64:67], v161
	ds_read_b128 v[84:87], v184
	ds_read_b128 v[68:71], v211
	ds_read_b128 v[88:91], v212
	ds_read_b128 v[72:75], v213
	ds_read_b128 v[92:95], v214
	ds_read_b128 v[76:79], v215
	v_max3_f32 v108, v108, v41, v60
	v_max3_f32 v109, v109, v62, v63
	v_max3_f32 v108, v108, v61, v44
	v_max3_f32 v109, v109, v46, v47
	v_max3_f32 v108, v108, v45, v109
	v_mov_b32_e32 v109, v108
	s_nop 1
	v_permlane32_swap_b32_e32 v108, v109
	v_max_f32_e32 v109, v109, v109
	v_max_f32_e32 v108, v108, v108
	v_max_f32_e32 v108, v108, v109
	s_mov_b32 s8, 0x3fb8aa3b
	v_fma_f32 v108, v108, s8, -v208
	s_mov_b32 s2, 0x41000000
	v_cmp_lt_f32_e32 vcc, s2, v108
	s_cmp_lg_u64 vcc, 0
	s_cselect_b64 s[2:3], -1, 0
	s_cbranch_vccnz .LBB3_39
.LBB3_28:
	s_waitcnt lgkmcnt(14)
	v_mfma_f32_32x32x16_f16 v[0:15], v[132:135], v[156:159], v[0:15]
	v_fma_f32 v48, v48, s8, -v208
	v_fma_f32 v49, v49, s8, -v208
	v_fma_f32 v50, v50, s8, -v208
	v_fma_f32 v51, v51, s8, -v208
	v_exp_f32_e32 v48, v48
	v_exp_f32_e32 v49, v49
	v_exp_f32_e32 v50, v50
	v_exp_f32_e32 v51, v51
	v_mfma_f32_32x32x16_f16 v[16:31], v[132:135], v[112:115], v[16:31]
	v_fma_f32 v52, v52, s8, -v208
	v_fma_f32 v53, v53, s8, -v208
	v_fma_f32 v54, v54, s8, -v208
	v_fma_f32 v55, v55, s8, -v208
	v_exp_f32_e32 v52, v52
	v_exp_f32_e32 v53, v53
	v_exp_f32_e32 v54, v54
	v_exp_f32_e32 v55, v55
	s_cmp_lg_u32 0, -1
	s_mov_b64 s[4:5], 0x540000
	s_cselect_b32 s9, 0, 0
	v_lshl_add_u64 v[108:109], v[162:163], 0, s[4:5]
	s_add_i32 s4, s9, s35
	s_add_i32 s4, s4, 0xa000
	s_mov_b32 m0, s4
	s_nop 0
	global_load_lds_dwordx4 v[108:109], off
	v_lshl_add_u64 v[226:227], v[108:109], 0, s[58:59]
	s_add_i32 m0, s4, 0x6800
	s_nop 0
	global_load_lds_dwordx4 v[226:227], off
	s_mov_b64 s[4:5], 0xf00
	s_waitcnt lgkmcnt(0)
	v_lshl_add_u64 v[108:109], v[164:165], 0, s[4:5]
	v_lshl_add_u64 v[108:109], v[108:109], 0, s[62:63]
	s_add_i32 m0, s36, s65
	s_nop 0
	global_load_lds_dwordx4 v[108:109], off nt
	ds_read_b128 v[112:115], v209 offset:16384
	ds_read_b128 v[116:119], v210 offset:16384
	v_mfma_f32_32x32x16_f16 v[0:15], v[128:131], v[104:107], v[0:15]
	v_fma_f32 v56, v56, s8, -v208
	v_fma_f32 v57, v57, s8, -v208
	v_fma_f32 v58, v58, s8, -v208
	v_fma_f32 v59, v59, s8, -v208
	v_exp_f32_e32 v56, v56
	v_exp_f32_e32 v57, v57
	v_exp_f32_e32 v58, v58
	v_exp_f32_e32 v59, v59
	s_add_i32 s7, s9, s7
	v_lshl_add_u64 v[104:105], v[178:179], 0, s[4:5]
	v_lshl_add_u64 v[104:105], v[104:105], 0, s[62:63]
	s_add_i32 s9, s7, 0x14c00
	s_add_i32 m0, s9, s65
	s_nop 0
	global_load_lds_dwordx4 v[104:105], off nt
	ds_read_b128 v[104:107], v209 offset:18432
	ds_read_b128 v[108:111], v210 offset:18432
	v_mfma_f32_32x32x16_f16 v[16:31], v[128:131], v[152:155], v[16:31]
	v_fma_f32 v60, v60, s8, -v208
	v_fma_f32 v61, v61, s8, -v208
	v_fma_f32 v62, v62, s8, -v208
	v_fma_f32 v63, v63, s8, -v208
	v_exp_f32_e32 v60, v60
	v_exp_f32_e32 v61, v61
	v_exp_f32_e32 v62, v62
	v_exp_f32_e32 v63, v63
	v_lshl_add_u64 v[128:129], v[176:177], 0, s[4:5]
	v_lshl_add_u64 v[128:129], v[128:129], 0, s[62:63]
	s_add_i32 s9, s7, 0x15000
	s_add_i32 m0, s9, s65
	s_nop 0
	global_load_lds_dwordx4 v[128:129], off nt
	v_mfma_f32_32x32x16_f16 v[0:15], v[124:127], v[148:151], v[0:15]
	v_fma_f32 v32, v32, s8, -v208
	v_fma_f32 v33, v33, s8, -v208
	v_fma_f32 v34, v34, s8, -v208
	v_fma_f32 v35, v35, s8, -v208
	v_exp_f32_e32 v32, v32
	v_exp_f32_e32 v33, v33
	v_exp_f32_e32 v34, v34
	v_exp_f32_e32 v35, v35
	v_lshl_add_u64 v[128:129], v[174:175], 0, s[4:5]
	v_lshl_add_u64 v[128:129], v[128:129], 0, s[62:63]
	s_add_i32 s9, s7, 0x15400
	s_add_i32 m0, s9, s65
	s_nop 0
	global_load_lds_dwordx4 v[128:129], off nt
	s_waitcnt lgkmcnt(14)
	v_mfma_f32_32x32x16_f16 v[16:31], v[124:127], v[144:147], v[16:31]
	v_fma_f32 v36, v36, s8, -v208
	v_fma_f32 v37, v37, s8, -v208
	v_fma_f32 v38, v38, s8, -v208
	v_fma_f32 v39, v39, s8, -v208
	v_exp_f32_e32 v36, v36
	v_exp_f32_e32 v37, v37
	v_exp_f32_e32 v38, v38
	v_exp_f32_e32 v39, v39
	s_add_i32 s9, s7, 0x15800
	v_mfma_f32_32x32x16_f16 v[0:15], v[120:123], v[140:143], v[0:15]
	v_fma_f32 v40, v40, s8, -v208
	v_fma_f32 v41, v41, s8, -v208
	v_fma_f32 v42, v42, s8, -v208
	v_fma_f32 v43, v43, s8, -v208
	v_exp_f32_e32 v40, v40
	v_exp_f32_e32 v41, v41
	v_exp_f32_e32 v42, v42
	v_exp_f32_e32 v43, v43
	s_add_i32 s9, s7, 0x15c00
	s_waitcnt lgkmcnt(12)
	v_mfma_f32_32x32x16_f16 v[16:31], v[120:123], v[136:139], v[16:31]
	v_fma_f32 v44, v44, s8, -v208
	v_fma_f32 v45, v45, s8, -v208
	v_fma_f32 v46, v46, s8, -v208
	v_fma_f32 v47, v47, s8, -v208
	v_exp_f32_e32 v44, v44
	v_exp_f32_e32 v45, v45
	v_exp_f32_e32 v46, v46
	v_exp_f32_e32 v47, v47
	s_add_i32 s8, s7, 0x16000
	s_add_i32 s7, s7, 0x16400
	s_waitcnt vmcnt(6) lgkmcnt(0)
	s_barrier
	s_andn2_b64 vcc, exec, s[2:3]
	s_cbranch_vccnz .LBB3_30
	ds_read_b128 v[136:139], v205 offset:49248
	ds_read_b128 v[140:143], v205 offset:49216
	ds_read_b128 v[144:147], v205 offset:49184
	ds_read_b128 v[148:151], v205 offset:49152
	s_waitcnt lgkmcnt(3)
	v_pk_mul_f32 v[14:15], v[14:15], v[138:139]
	s_waitcnt lgkmcnt(2)
	v_pk_mul_f32 v[10:11], v[10:11], v[142:143]
	s_waitcnt lgkmcnt(1)
	v_pk_mul_f32 v[6:7], v[6:7], v[146:147]
	s_waitcnt lgkmcnt(0)
	v_pk_mul_f32 v[2:3], v[2:3], v[150:151]
	v_pk_mul_f32 v[12:13], v[12:13], v[136:137]
	v_pk_mul_f32 v[8:9], v[8:9], v[140:141]
	v_pk_mul_f32 v[4:5], v[4:5], v[144:145]
	v_pk_mul_f32 v[0:1], v[0:1], v[148:149]
	v_pk_mul_f32 v[30:31], v[30:31], v[138:139]
	v_pk_mul_f32 v[26:27], v[26:27], v[142:143]
	v_pk_mul_f32 v[22:23], v[22:23], v[146:147]
	v_pk_mul_f32 v[18:19], v[18:19], v[150:151]
	v_pk_mul_f32 v[28:29], v[28:29], v[136:137]
	v_pk_mul_f32 v[24:25], v[24:25], v[140:141]
	v_pk_mul_f32 v[20:21], v[20:21], v[144:145]
	v_pk_mul_f32 v[16:17], v[16:17], v[148:149]
.LBB3_30:
	ds_read_b64_tr_b16 v[152:153], v207 offset:32768
	ds_read_b64_tr_b16 v[154:155], v207 offset:33280
	v_add_f32_e32 v120, v48, v49
	v_mov_b32_e32 v121, 0x7f7f7f7f
	v_mov_b32_e32 v124, 0x7c7c7c7c
	s_waitcnt lgkmcnt(4)
	v_mfma_scale_f32_32x32x64_f8f6f4 v[80:95], v[112:119], v[96:103], v[80:95], v121, v124 op_sel_hi:[0,0,0]
	v_add_f32_e32 v112, v50, v120
	v_add_f32_e32 v112, v51, v112
	v_add_f32_e32 v112, v52, v112
	v_add_f32_e32 v116, v53, v112
	v_cvt_pk_f16_f32 v132, v48, v49
	v_cvt_pk_f16_f32 v133, v50, v51
	ds_read_b64_tr_b16 v[112:113], v207 offset:36864
	ds_read_b64_tr_b16 v[114:115], v207 offset:37376
	v_add_f32_e32 v48, v54, v116
	v_add_f32_e32 v48, v55, v48
	v_add_f32_e32 v48, v56, v48
	v_add_f32_e32 v48, v57, v48
	v_cvt_pk_f16_f32 v134, v52, v53
	v_cvt_pk_f16_f32 v135, v54, v55
	s_waitcnt lgkmcnt(4)
	v_mfma_scale_f32_32x32x64_f8f6f4 v[64:79], v[104:111], v[96:103], v[64:79], v121, v124 op_sel_hi:[0,0,0]
	ds_read_b64_tr_b16 v[104:105], v207 offset:33792
	ds_read_b64_tr_b16 v[106:107], v207 offset:34304
	v_add_f32_e32 v48, v58, v48
	v_add_f32_e32 v48, v59, v48
	v_add_f32_e32 v48, v60, v48
	v_add_f32_e32 v48, v61, v48
	v_cvt_pk_f16_f32 v128, v56, v57
	v_cvt_pk_f16_f32 v129, v58, v59
	ds_read_b64_tr_b16 v[156:157], v207 offset:37888
	ds_read_b64_tr_b16 v[158:159], v207 offset:38400
	v_add_f32_e32 v48, v62, v48
	v_add_f32_e32 v48, v63, v48
	v_add_f32_e32 v48, v32, v48
	v_add_f32_e32 v48, v33, v48
	v_cvt_pk_f16_f32 v130, v60, v61
	v_cvt_pk_f16_f32 v131, v62, v63
	ds_read_b64_tr_b16 v[148:149], v207 offset:34816
	ds_read_b64_tr_b16 v[150:151], v207 offset:35328
	v_add_f32_e32 v48, v34, v48
	v_add_f32_e32 v48, v35, v48
	v_add_f32_e32 v48, v36, v48
	v_add_f32_e32 v48, v37, v48
	v_cvt_pk_f16_f32 v124, v32, v33
	v_cvt_pk_f16_f32 v125, v34, v35
	ds_read_b64_tr_b16 v[144:145], v207 offset:38912
	ds_read_b64_tr_b16 v[146:147], v207 offset:39424
	v_add_f32_e32 v32, v38, v48
	v_add_f32_e32 v32, v39, v32
	v_add_f32_e32 v32, v40, v32
	v_add_f32_e32 v32, v41, v32
	v_cvt_pk_f16_f32 v126, v36, v37
	v_cvt_pk_f16_f32 v127, v38, v39
	ds_read_b64_tr_b16 v[140:141], v207 offset:35840
	ds_read_b64_tr_b16 v[142:143], v207 offset:36352
	v_add_f32_e32 v32, v42, v32
	v_add_f32_e32 v32, v43, v32
	v_add_f32_e32 v32, v44, v32
	v_add_f32_e32 v32, v45, v32
	v_cvt_pk_f16_f32 v120, v40, v41
	v_cvt_pk_f16_f32 v121, v42, v43
	ds_read_b64_tr_b16 v[136:137], v207 offset:39936
	ds_read_b64_tr_b16 v[138:139], v207 offset:40448
	v_add_f32_e32 v32, v46, v32
	v_add_f32_e32 v32, v47, v32
	v_add_f32_e32 v32, 0, v32
	v_cvt_pk_f16_f32 v122, v44, v45
	v_cvt_pk_f16_f32 v123, v46, v47
	s_nop 1
	s_waitcnt vmcnt(0)
	s_barrier
	s_nop 0
	v_add_f32_e32 v164, v180, v32
	v_max_f32_e32 v108, v81, v81
	v_max_f32_e32 v109, v80, v80
	v_max_f32_e32 v108, v109, v108
	v_max3_f32 v109, v82, v83, v65
	v_max3_f32 v108, v108, v64, v66
	v_max3_f32 v108, v108, v67, v84
	v_max3_f32 v109, v109, v86, v87
	v_max3_f32 v108, v108, v85, v68
	v_max3_f32 v109, v109, v70, v71
	v_max3_f32 v108, v108, v69, v88
	v_max3_f32 v109, v109, v90, v91
	v_max3_f32 v108, v108, v89, v72
	v_max3_f32 v109, v109, v74, v75
	ds_read_b128 v[48:51], v221 offset:32768
	ds_read_b128 v[32:35], v161 offset:32768
	ds_read_b128 v[52:55], v184 offset:32768
	ds_read_b128 v[36:39], v211 offset:32768
	ds_read_b128 v[56:59], v212 offset:32768
	ds_read_b128 v[40:43], v213 offset:32768
	ds_read_b128 v[60:63], v214 offset:32768
	ds_read_b128 v[44:47], v215 offset:32768
	v_max3_f32 v108, v108, v73, v92
	v_max3_f32 v109, v109, v94, v95
	v_max3_f32 v108, v108, v93, v76
	v_max3_f32 v109, v109, v78, v79
	v_max3_f32 v108, v108, v77, v109
	v_mov_b32_e32 v109, v108
	s_nop 1
	v_permlane32_swap_b32_e32 v108, v109
	v_max_f32_e32 v109, v109, v109
	v_max_f32_e32 v108, v108, v108
	v_max_f32_e32 v108, v108, v109
	s_mov_b32 s7, 0x3fb8aa3b
	v_fma_f32 v108, v108, s7, -v208
	s_mov_b32 s2, 0x41000000
	v_cmp_lt_f32_e32 vcc, s2, v108
	s_cmp_lg_u64 vcc, 0
	s_cselect_b64 s[2:3], -1, 0
	s_cbranch_vccnz .LBB3_42
.LBB3_31:
	s_waitcnt lgkmcnt(14)
	v_mfma_f32_32x32x16_f16 v[0:15], v[132:135], v[152:155], v[0:15]
	v_fma_f32 v80, v80, s7, -v208
	v_fma_f32 v81, v81, s7, -v208
	v_fma_f32 v82, v82, s7, -v208
	v_fma_f32 v83, v83, s7, -v208
	v_exp_f32_e32 v80, v80
	v_exp_f32_e32 v81, v81
	v_exp_f32_e32 v82, v82
	v_exp_f32_e32 v83, v83
	v_mfma_f32_32x32x16_f16 v[16:31], v[132:135], v[112:115], v[16:31]
	v_fma_f32 v84, v84, s7, -v208
	v_fma_f32 v85, v85, s7, -v208
	v_fma_f32 v86, v86, s7, -v208
	v_fma_f32 v87, v87, s7, -v208
	v_exp_f32_e32 v84, v84
	v_exp_f32_e32 v85, v85
	v_exp_f32_e32 v86, v86
	v_exp_f32_e32 v87, v87
	s_mov_b64 s[4:5], 0x5a0000
	v_lshl_add_u64 v[108:109], v[162:163], 0, s[4:5]
	s_mov_b32 m0, s34
	s_nop 0
	global_load_lds_dwordx4 v[108:109], off
	v_lshl_add_u64 v[226:227], v[108:109], 0, s[58:59]
	s_add_i32 m0, s34, 0x6800
	s_nop 0
	global_load_lds_dwordx4 v[226:227], off
	ds_read_b128 v[112:115], v209
	ds_read_b128 v[116:119], v210
	v_mfma_f32_32x32x16_f16 v[0:15], v[128:131], v[104:107], v[0:15]
	v_fma_f32 v88, v88, s7, -v208
	v_fma_f32 v89, v89, s7, -v208
	v_fma_f32 v90, v90, s7, -v208
	v_fma_f32 v91, v91, s7, -v208
	v_exp_f32_e32 v88, v88
	v_exp_f32_e32 v89, v89
	v_exp_f32_e32 v90, v90
	v_exp_f32_e32 v91, v91
	ds_read_b128 v[104:107], v209 offset:2048
	ds_read_b128 v[108:111], v210 offset:2048
	v_mfma_f32_32x32x16_f16 v[16:31], v[128:131], v[156:159], v[16:31]
	v_fma_f32 v92, v92, s7, -v208
	v_fma_f32 v93, v93, s7, -v208
	v_fma_f32 v94, v94, s7, -v208
	v_fma_f32 v95, v95, s7, -v208
	v_exp_f32_e32 v92, v92
	v_exp_f32_e32 v93, v93
	v_exp_f32_e32 v94, v94
	v_exp_f32_e32 v95, v95
	v_mfma_f32_32x32x16_f16 v[0:15], v[124:127], v[148:151], v[0:15]
	v_fma_f32 v64, v64, s7, -v208
	v_fma_f32 v65, v65, s7, -v208
	v_fma_f32 v66, v66, s7, -v208
	v_fma_f32 v67, v67, s7, -v208
	v_exp_f32_e32 v64, v64
	v_exp_f32_e32 v65, v65
	v_exp_f32_e32 v66, v66
	v_exp_f32_e32 v67, v67
	s_waitcnt lgkmcnt(14)
	v_mfma_f32_32x32x16_f16 v[16:31], v[124:127], v[144:147], v[16:31]
	v_fma_f32 v68, v68, s7, -v208
	v_fma_f32 v69, v69, s7, -v208
	v_fma_f32 v70, v70, s7, -v208
	v_fma_f32 v71, v71, s7, -v208
	v_exp_f32_e32 v68, v68
	v_exp_f32_e32 v69, v69
	v_exp_f32_e32 v70, v70
	v_exp_f32_e32 v71, v71
	v_mfma_f32_32x32x16_f16 v[0:15], v[120:123], v[140:143], v[0:15]
	v_fma_f32 v72, v72, s7, -v208
	v_fma_f32 v73, v73, s7, -v208
	v_fma_f32 v74, v74, s7, -v208
	v_fma_f32 v75, v75, s7, -v208
	v_exp_f32_e32 v72, v72
	v_exp_f32_e32 v73, v73
	v_exp_f32_e32 v74, v74
	v_exp_f32_e32 v75, v75
	s_waitcnt lgkmcnt(12)
	v_mfma_f32_32x32x16_f16 v[16:31], v[120:123], v[136:139], v[16:31]
	v_fma_f32 v76, v76, s7, -v208
	v_fma_f32 v77, v77, s7, -v208
	v_fma_f32 v78, v78, s7, -v208
	v_fma_f32 v79, v79, s7, -v208
	v_exp_f32_e32 v76, v76
	v_exp_f32_e32 v77, v77
	v_exp_f32_e32 v78, v78
	v_exp_f32_e32 v79, v79
	s_waitcnt vmcnt(0) lgkmcnt(0)
	s_barrier
	s_andn2_b64 vcc, exec, s[2:3]
	s_cbranch_vccnz .LBB3_33
	ds_read_b128 v[136:139], v205 offset:49248
	ds_read_b128 v[140:143], v205 offset:49216
	ds_read_b128 v[144:147], v205 offset:49184
	ds_read_b128 v[148:151], v205 offset:49152
	s_waitcnt lgkmcnt(3)
	v_pk_mul_f32 v[14:15], v[14:15], v[138:139]
	s_waitcnt lgkmcnt(2)
	v_pk_mul_f32 v[10:11], v[10:11], v[142:143]
	s_waitcnt lgkmcnt(1)
	v_pk_mul_f32 v[6:7], v[6:7], v[146:147]
	s_waitcnt lgkmcnt(0)
	v_pk_mul_f32 v[2:3], v[2:3], v[150:151]
	v_pk_mul_f32 v[12:13], v[12:13], v[136:137]
	v_pk_mul_f32 v[8:9], v[8:9], v[140:141]
	v_pk_mul_f32 v[4:5], v[4:5], v[144:145]
	v_pk_mul_f32 v[0:1], v[0:1], v[148:149]
	v_pk_mul_f32 v[30:31], v[30:31], v[138:139]
	v_pk_mul_f32 v[26:27], v[26:27], v[142:143]
	v_pk_mul_f32 v[22:23], v[22:23], v[146:147]
	v_pk_mul_f32 v[18:19], v[18:19], v[150:151]
	v_pk_mul_f32 v[28:29], v[28:29], v[136:137]
	v_pk_mul_f32 v[24:25], v[24:25], v[140:141]
	v_pk_mul_f32 v[20:21], v[20:21], v[144:145]
	v_pk_mul_f32 v[16:17], v[16:17], v[148:149]

.LBB3_36:
	v_add_f32_e32 v64, v48, v49
	v_add_f32_e32 v64, v50, v64
	v_add_f32_e32 v64, v51, v64
	v_add_f32_e32 v64, v52, v64
	v_add_f32_e32 v68, v53, v64
	v_cvt_pk_f16_f32 v48, v48, v49
	v_cvt_pk_f16_f32 v49, v50, v51
	v_cvt_pk_f16_f32 v50, v52, v53
	v_cvt_pk_f16_f32 v51, v54, v55
	ds_read_b64_tr_b16 v[64:65], v207 offset:24576
	ds_read_b64_tr_b16 v[66:67], v207 offset:25088
	v_add_f32_e32 v52, v54, v68
	v_add_f32_e32 v68, v55, v52
	ds_read_b64_tr_b16 v[52:53], v207 offset:25600
	ds_read_b64_tr_b16 v[54:55], v207 offset:26112
	s_waitcnt lgkmcnt(2)
	v_mfma_f32_32x32x16_f16 v[0:15], v[48:51], v[64:67], v[0:15]
	ds_read_b64_tr_b16 v[64:65], v207 offset:28672
	ds_read_b64_tr_b16 v[66:67], v207 offset:29184
	v_add_f32_e32 v68, v56, v68
	v_add_f32_e32 v73, v57, v68
	v_cvt_pk_f16_f32 v68, v56, v57
	v_cvt_pk_f16_f32 v69, v58, v59
	v_cvt_pk_f16_f32 v70, v60, v61
	v_cvt_pk_f16_f32 v71, v62, v63
	s_waitcnt lgkmcnt(0)
	v_mfma_f32_32x32x16_f16 v[16:31], v[48:51], v[64:67], v[16:31]
	v_add_f32_e32 v48, v58, v73
	v_add_f32_e32 v48, v59, v48
	v_add_f32_e32 v48, v60, v48
	v_add_f32_e32 v48, v61, v48
	ds_read_b64_tr_b16 v[74:75], v207 offset:29696
	ds_read_b64_tr_b16 v[76:77], v207 offset:30208
	v_add_f32_e32 v48, v62, v48
	v_add_f32_e32 v48, v63, v48
	v_mfma_f32_32x32x16_f16 v[0:15], v[68:71], v[52:55], v[0:15]
	v_add_f32_e32 v48, v32, v48
	v_add_f32_e32 v56, v33, v48
	v_cvt_pk_f16_f32 v48, v32, v33
	v_cvt_pk_f16_f32 v49, v34, v35
	v_cvt_pk_f16_f32 v50, v36, v37
	v_cvt_pk_f16_f32 v51, v38, v39
	ds_read_b64_tr_b16 v[52:53], v207 offset:26624
	ds_read_b64_tr_b16 v[54:55], v207 offset:27136
	s_waitcnt lgkmcnt(2)
	v_mfma_f32_32x32x16_f16 v[16:31], v[68:71], v[74:77], v[16:31]
	v_add_f32_e32 v32, v34, v56
	v_add_f32_e32 v56, v35, v32
	ds_read_b64_tr_b16 v[32:33], v207 offset:27648
	ds_read_b64_tr_b16 v[34:35], v207 offset:28160
	v_add_f32_e32 v36, v36, v56
	v_add_f32_e32 v36, v37, v36
	v_cvt_pk_f16_f32 v56, v40, v41
	v_cvt_pk_f16_f32 v57, v42, v43
	s_waitcnt lgkmcnt(2)
	v_mfma_f32_32x32x16_f16 v[0:15], v[48:51], v[52:55], v[0:15]
	ds_read_b64_tr_b16 v[52:53], v207 offset:30720
	ds_read_b64_tr_b16 v[54:55], v207 offset:31232
	v_cvt_pk_f16_f32 v58, v44, v45
	v_cvt_pk_f16_f32 v59, v46, v47
	ds_read_b64_tr_b16 v[60:61], v207 offset:31744
	ds_read_b64_tr_b16 v[62:63], v207 offset:32256
	v_add_f32_e32 v36, v38, v36
	v_add_f32_e32 v36, v39, v36
	v_add_f32_e32 v36, v40, v36
	s_waitcnt lgkmcnt(2)
	v_mfma_f32_32x32x16_f16 v[16:31], v[48:51], v[52:55], v[16:31]
	v_add_f32_e32 v36, v41, v36
	v_mfma_f32_32x32x16_f16 v[0:15], v[56:59], v[32:35], v[0:15]
	v_add_f32_e32 v32, v42, v36
	v_add_f32_e32 v32, v43, v32
	v_add_f32_e32 v32, v44, v32
	v_add_f32_e32 v32, v45, v32
	v_add_f32_e32 v32, v46, v32
	v_add_f32_e32 v32, v47, v32
	v_add_f32_e32 v32, v72, v32
	s_waitcnt lgkmcnt(0)
	v_mfma_f32_32x32x16_f16 v[16:31], v[56:59], v[60:63], v[16:31]
	v_mov_b32_e32 v33, v32
	s_nop 1
	v_permlane32_swap_b32_e32 v32, v33
	s_and_saveexec_b64 s[2:3], s[0:1]
	v_add_f32_e32 v32, v32, v33
	ds_write_b32 v206, v32 offset:49280
	s_or_b64 exec, exec, s[2:3]
	s_waitcnt lgkmcnt(0)
	ds_read_b128 v[32:35], v205 offset:49280
	ds_read_b128 v[36:39], v205 offset:49312
	s_lshl_b64 s[0:1], s[18:19], 10
	s_add_u32 s0, s16, s0
	s_addc_u32 s1, s17, s1
	s_waitcnt lgkmcnt(1)
	v_rcp_f32_e32 v40, v32
	v_rcp_f32_e32 v41, v33
	v_rcp_f32_e32 v42, v34
	s_lshl_b32 s2, s33, 11
	v_mul_f32_e32 v40, 0x41800000, v40
	v_mul_f32_e32 v0, v0, v40
	v_mul_f32_e32 v16, v16, v40
	v_mov_b32_e32 v40, 0
	v_cvt_pk_fp8_f32 v40, v0, v16
	v_mul_f32_e32 v16, 0x41800000, v41
	v_mul_f32_e32 v1, v1, v16
	v_mul_f32_e32 v16, v17, v16
	v_mov_b32_e32 v17, 0
	v_cvt_pk_fp8_f32 v17, v1, v16
	s_add_i32 s2, s2, 0
	v_lshlrev_b32_e32 v0, 8, v204
	v_rcp_f32_e32 v43, v35
	v_add3_u32 v0, s2, v203, v0
	v_lshrrev_b32_e32 v1, 8, v40
	s_waitcnt lgkmcnt(0)
	v_rcp_f32_e32 v44, v36
	ds_read_b128 v[32:35], v205 offset:49344
	v_rcp_f32_e32 v45, v37
	v_rcp_f32_e32 v46, v38
	v_rcp_f32_e32 v47, v39
	ds_read_b128 v[36:39], v205 offset:49376
	s_waitcnt lgkmcnt(0)
	s_barrier
	ds_write_b8 v0, v40 offset:51200
	ds_write_b8 v0, v1 offset:51232
	ds_write_b8 v0, v17 offset:51264
	v_lshrrev_b32_e32 v1, 8, v17
	ds_write_b8 v0, v1 offset:51296
	v_mul_f32_e32 v1, 0x41800000, v42
	v_mul_f32_e32 v2, v2, v1
	v_mul_f32_e32 v1, v18, v1
	v_mov_b32_e32 v16, 0
	v_cvt_pk_fp8_f32 v16, v2, v1
	v_mul_f32_e32 v1, 0x41800000, v43
	v_mul_f32_e32 v2, v3, v1
	v_mul_f32_e32 v1, v19, v1
	v_mov_b32_e32 v3, 0
	v_cvt_pk_fp8_f32 v3, v2, v1
	v_lshrrev_b32_e32 v1, 8, v16
	ds_write_b8 v0, v16 offset:51328
	ds_write_b8 v0, v1 offset:51360
	ds_write_b8 v0, v3 offset:51392
	v_lshrrev_b32_e32 v1, 8, v3
	ds_write_b8 v0, v1 offset:51424
	v_mul_f32_e32 v1, 0x41800000, v44
	v_mul_f32_e32 v2, v4, v1
	v_mul_f32_e32 v1, v20, v1
	v_mov_b32_e32 v3, 0
	v_cvt_pk_fp8_f32 v3, v2, v1
	v_mul_f32_e32 v1, 0x41800000, v45
	v_mul_f32_e32 v2, v5, v1
	v_mul_f32_e32 v1, v21, v1
	v_mov_b32_e32 v4, 0
	v_cvt_pk_fp8_f32 v4, v2, v1
	v_lshrrev_b32_e32 v1, 8, v3
	ds_write_b8 v0, v3 offset:51712
	ds_write_b8 v0, v1 offset:51744
	ds_write_b8 v0, v4 offset:51776
	v_lshrrev_b32_e32 v1, 8, v4
	ds_write_b8 v0, v1 offset:51808
	v_mul_f32_e32 v1, 0x41800000, v46
	v_mul_f32_e32 v2, v6, v1
	v_mul_f32_e32 v1, v22, v1
	v_mov_b32_e32 v3, 0
	v_cvt_pk_fp8_f32 v3, v2, v1
	v_mul_f32_e32 v1, 0x41800000, v47
	v_mul_f32_e32 v2, v7, v1
	v_mul_f32_e32 v1, v23, v1
	v_mov_b32_e32 v4, 0
	v_cvt_pk_fp8_f32 v4, v2, v1
	s_waitcnt lgkmcnt(13)
	v_rcp_f32_e32 v32, v32
	v_rcp_f32_e32 v33, v33
	v_lshrrev_b32_e32 v1, 8, v3
	ds_write_b8 v0, v3 offset:51840
	ds_write_b8 v0, v1 offset:51872
	ds_write_b8 v0, v4 offset:51904
	v_lshrrev_b32_e32 v1, 8, v4
	ds_write_b8 v0, v1 offset:51936
	v_mul_f32_e32 v1, 0x41800000, v32
	v_mul_f32_e32 v2, v8, v1
	v_mul_f32_e32 v1, v24, v1
	v_mov_b32_e32 v3, 0
	v_cvt_pk_fp8_f32 v3, v2, v1
	v_mul_f32_e32 v1, 0x41800000, v33
	v_mul_f32_e32 v2, v9, v1
	v_mul_f32_e32 v1, v25, v1
	v_mov_b32_e32 v4, 0
	v_cvt_pk_fp8_f32 v4, v2, v1
	v_rcp_f32_e32 v34, v34
	v_rcp_f32_e32 v35, v35
	v_lshrrev_b32_e32 v1, 8, v3
	ds_write_b8 v0, v3 offset:52224
	ds_write_b8 v0, v1 offset:52256
	ds_write_b8 v0, v4 offset:52288
	v_lshrrev_b32_e32 v1, 8, v4
	ds_write_b8 v0, v1 offset:52320
	v_mul_f32_e32 v1, 0x41800000, v34
	v_mul_f32_e32 v2, v10, v1
	v_mul_f32_e32 v1, v26, v1
	v_mov_b32_e32 v3, 0
	v_cvt_pk_fp8_f32 v3, v2, v1
	v_mul_f32_e32 v1, 0x41800000, v35
	v_mul_f32_e32 v2, v11, v1
	v_mul_f32_e32 v1, v27, v1
	v_mov_b32_e32 v4, 0
	v_cvt_pk_fp8_f32 v4, v2, v1
	s_waitcnt lgkmcnt(14)
	v_rcp_f32_e32 v36, v36
	v_rcp_f32_e32 v37, v37
	v_lshrrev_b32_e32 v1, 8, v3
	ds_write_b8 v0, v3 offset:52352
	ds_write_b8 v0, v1 offset:52384
	ds_write_b8 v0, v4 offset:52416
	v_lshrrev_b32_e32 v1, 8, v4
	ds_write_b8 v0, v1 offset:52448
	v_mul_f32_e32 v1, 0x41800000, v36
	v_mul_f32_e32 v2, v12, v1
	v_mul_f32_e32 v1, v28, v1
	v_mov_b32_e32 v3, 0
	v_cvt_pk_fp8_f32 v3, v2, v1
	v_mul_f32_e32 v1, 0x41800000, v37
	v_mul_f32_e32 v2, v13, v1
	v_mul_f32_e32 v1, v29, v1
	v_mov_b32_e32 v4, 0
	v_cvt_pk_fp8_f32 v4, v2, v1
	v_rcp_f32_e32 v38, v38
	v_rcp_f32_e32 v39, v39
	v_lshrrev_b32_e32 v1, 8, v3
	ds_write_b8 v0, v3 offset:52736
	ds_write_b8 v0, v1 offset:52768
	ds_write_b8 v0, v4 offset:52800
	v_lshrrev_b32_e32 v1, 8, v4
	ds_write_b8 v0, v1 offset:52832
	v_mul_f32_e32 v1, 0x41800000, v38
	v_mul_f32_e32 v2, v14, v1
	v_mul_f32_e32 v1, v30, v1
	v_mov_b32_e32 v3, 0
	v_cvt_pk_fp8_f32 v3, v2, v1
	v_mul_f32_e32 v1, 0x41800000, v39
	v_mul_f32_e32 v2, v15, v1
	v_mul_f32_e32 v1, v31, v1
	v_mov_b32_e32 v4, 0
	v_cvt_pk_fp8_f32 v4, v2, v1
	v_lshrrev_b32_e32 v1, 8, v3
	ds_write_b8 v0, v3 offset:52864
	ds_write_b8 v0, v1 offset:52896
	ds_write_b8 v0, v4 offset:52928
	v_lshrrev_b32_e32 v1, 8, v4
	ds_write_b8 v0, v1 offset:52960
	v_add_u32_e32 v4, s2, v160
	s_waitcnt lgkmcnt(0)
	v_lshl_add_u32 v0, v202, 6, v4
	v_or_b32_e32 v12, 16, v202
	ds_read_b128 v[0:3], v0 offset:51200
	v_lshl_add_u32 v4, v12, 6, v4
	s_add_u32 s0, s0, s6
	ds_read_b128 v[4:7], v4 offset:51200
	v_mov_b32_e32 v161, 0
	s_addc_u32 s1, s1, 0
	v_lshl_add_u64 v[8:9], s[0:1], 0, v[160:161]
	v_lshlrev_b32_e32 v160, 10, v202
	v_lshl_add_u64 v[10:11], v[8:9], 0, v[160:161]
	v_lshlrev_b32_e32 v160, 10, v12
	s_waitcnt lgkmcnt(1)
	global_store_dwordx4 v[10:11], v[0:3], off
	s_nop 1
	v_lshl_add_u64 v[0:1], v[8:9], 0, v[160:161]
	s_waitcnt lgkmcnt(0)
	global_store_dwordx4 v[0:1], v[4:7], off
	s_waitcnt lgkmcnt(0)
	s_barrier
	s_endpgm

	.amdhsa_kernel _Z6k_attnILi1024ELi1024ELi1024ELi1024ELi3072ELi1024ELb1ELb1EEvPKDF16_S1_S1_PKfPDF16_
		.amdhsa_group_segment_fixed_size 0
		.amdhsa_private_segment_fixed_size 0
		.amdhsa_kernarg_size 40
		.amdhsa_user_sgpr_count 2
		.amdhsa_user_sgpr_dispatch_ptr 0
		.amdhsa_user_sgpr_queue_ptr 0
		.amdhsa_user_sgpr_kernarg_segment_ptr 1
		.amdhsa_user_sgpr_dispatch_id 0
		.amdhsa_user_sgpr_kernarg_preload_length 0
		.amdhsa_user_sgpr_kernarg_preload_offset 0
		.amdhsa_user_sgpr_private_segment_size 0
		.amdhsa_uses_dynamic_stack 0
		.amdhsa_enable_private_segment 0
		.amdhsa_system_sgpr_workgroup_id_x 1
		.amdhsa_system_sgpr_workgroup_id_y 0
		.amdhsa_system_sgpr_workgroup_id_z 0
		.amdhsa_system_sgpr_workgroup_info 0
		.amdhsa_system_vgpr_workitem_id 0
		.amdhsa_next_free_vgpr 240
		.amdhsa_next_free_sgpr 66
		.amdhsa_accum_offset 240
		.amdhsa_reserve_vcc 1
		.amdhsa_float_round_mode_32 0
		.amdhsa_float_round_mode_16_64 0
		.amdhsa_float_denorm_mode_32 3
		.amdhsa_float_denorm_mode_16_64 3
		.amdhsa_dx10_clamp 1
		.amdhsa_ieee_mode 1
		.amdhsa_fp16_overflow 0
		.amdhsa_tg_split 0
		.amdhsa_exception_fp_ieee_invalid_op 0
		.amdhsa_exception_fp_denorm_src 0
		.amdhsa_exception_fp_ieee_div_zero 0
		.amdhsa_exception_fp_ieee_overflow 0
		.amdhsa_exception_fp_ieee_underflow 0
		.amdhsa_exception_fp_ieee_inexact 0
		.amdhsa_exception_int_div_zero 0
	.end_amdhsa_kernel

amdhsa.kernels:
  - .agpr_count:     0
    .args:
      - .offset:         0
        .size:           384
        .value_kind:     by_value
    .group_segment_fixed_size: 5120
    .kernarg_segment_align: 8
    .kernarg_segment_size: 384
    .language:       OpenCL C
    .language_version:
      - 2
      - 0
    .max_flat_workgroup_size: 256
    .name:           _Z6k_prep6WtArgs
    .private_segment_fixed_size: 0
    .sgpr_count:     38
    .sgpr_spill_count: 0
    .symbol:         _Z6k_prep6WtArgs.kd
    .uniform_work_group_size: 1
    .uses_dynamic_stack: false
    .vgpr_count:     29
    .vgpr_spill_count: 0
    .wavefront_size: 64
  - .agpr_count:     0
    .args:
      - .actual_access:  read_only
        .address_space:  global
        .offset:         0
        .size:           8
        .value_kind:     global_buffer
      - .actual_access:  read_only
        .address_space:  global
        .offset:         8
        .size:           8
        .value_kind:     global_buffer
      - .actual_access:  read_only
        .address_space:  global
        .offset:         16
        .size:           8
        .value_kind:     global_buffer
      - .actual_access:  write_only
        .address_space:  global
        .offset:         24
        .size:           8
        .value_kind:     global_buffer
      - .actual_access:  write_only
        .address_space:  global
        .offset:         32
        .size:           8
        .value_kind:     global_buffer
      - .actual_access:  write_only
        .address_space:  global
        .offset:         40
        .size:           8
        .value_kind:     global_buffer
      - .offset:         48
        .size:           4
        .value_kind:     by_value
    .group_segment_fixed_size: 0
    .kernarg_segment_align: 8
    .kernarg_segment_size: 52
    .language:       OpenCL C
    .language_version:
      - 2
      - 0
    .max_flat_workgroup_size: 256
    .name:           _Z4k_lnPKDF16_PKfS2_PfPDF16_Phi
    .private_segment_fixed_size: 0
    .sgpr_count:     18
    .sgpr_spill_count: 0
    .symbol:         _Z4k_lnPKDF16_PKfS2_PfPDF16_Phi.kd
    .uniform_work_group_size: 1
    .uses_dynamic_stack: false
    .vgpr_count:     59
    .vgpr_spill_count: 0
    .wavefront_size: 64
  - .agpr_count:     0
    .args:
      - .offset:         0
        .size:           56
        .value_kind:     by_value
      - .offset:         56
        .size:           72
        .value_kind:     by_value
      - .offset:         128
        .size:           176
        .value_kind:     by_value
      - .address_space:  global
        .offset:         304
        .size:           8
        .value_kind:     global_buffer
      - .offset:         312
        .size:           4
        .value_kind:     hidden_block_count_x
      - .offset:         316
        .size:           4
        .value_kind:     hidden_block_count_y
      - .offset:         320
        .size:           4
        .value_kind:     hidden_block_count_z
      - .offset:         324
        .size:           2
        .value_kind:     hidden_group_size_x
      - .offset:         326
        .size:           2
        .value_kind:     hidden_group_size_y
      - .offset:         328
        .size:           2
        .value_kind:     hidden_group_size_z
      - .offset:         330
        .size:           2
        .value_kind:     hidden_remainder_x
      - .offset:         332
        .size:           2
        .value_kind:     hidden_remainder_y
      - .offset:         334
        .size:           2
        .value_kind:     hidden_remainder_z
      - .offset:         352
        .size:           8
        .value_kind:     hidden_global_offset_x
      - .offset:         360
        .size:           8
        .value_kind:     hidden_global_offset_y
      - .offset:         368
        .size:           8
        .value_kind:     hidden_global_offset_z
      - .offset:         376
        .size:           2
        .value_kind:     hidden_grid_dims
      - .offset:         432
        .size:           4
        .value_kind:     hidden_dynamic_lds_size
    .group_segment_fixed_size: 0
    .kernarg_segment_align: 8
    .kernarg_segment_size: 568
    .language:       OpenCL C
    .language_version:
      - 2
      - 0
    .max_flat_workgroup_size: 512
    .name:           _Z6k_gemmIN3pg84EpiHILi0ELb1EEELb1EEvNS0_4GemmET_6WtTailPj
    .private_segment_fixed_size: 0
    .sgpr_count:     72
    .sgpr_spill_count: 5
    .symbol:         _Z6k_gemmIN3pg84EpiHILi0ELb1EEELb1EEvNS0_4GemmET_6WtTailPj.kd
    .uniform_work_group_size: 1
    .uses_dynamic_stack: false
    .vgpr_count:     240
    .vgpr_spill_count: 0
    .wavefront_size: 64
  - .agpr_count:     0
    .args:
      - .address_space:  global
        .offset:         0
        .size:           8
        .value_kind:     global_buffer
      - .address_space:  global
        .offset:         8
        .size:           8
        .value_kind:     global_buffer
      - .address_space:  global
        .offset:         16
        .size:           8
        .value_kind:     global_buffer
      - .address_space:  global
        .offset:         24
        .size:           8
        .value_kind:     global_buffer
      - .address_space:  global
        .offset:         32
        .size:           8
        .value_kind:     global_buffer
    .group_segment_fixed_size: 0
    .kernarg_segment_align: 8
    .kernarg_segment_size: 40
    .language:       OpenCL C
    .language_version:
      - 2
      - 0
    .max_flat_workgroup_size: 512
    .name:           _Z6k_attnILi1024ELi1024ELi1024ELi1024ELi3072ELi1024ELb1ELb1EEvPKDF16_S1_S1_PKfPDF16_
    .private_segment_fixed_size: 0
    .sgpr_count:     55
    .sgpr_spill_count: 0
    .symbol:         _Z6k_attnILi1024ELi1024ELi1024ELi1024ELi3072ELi1024ELb1ELb1EEvPKDF16_S1_S1_PKfPDF16_.kd
    .uniform_work_group_size: 1
    .uses_dynamic_stack: false
    .vgpr_count:     224
    .vgpr_spill_count: 0
    .wavefront_size: 64
  - .agpr_count:     0
    .args:
      - .address_space:  global
        .offset:         0
        .size:           8
        .value_kind:     global_buffer
      - .address_space:  global
        .offset:         8
        .size:           8
        .value_kind:     global_buffer
      - .offset:         16
        .size:           4
        .value_kind:     by_value
      - .offset:         20
        .size:           4
        .value_kind:     by_value
      - .offset:         24
        .size:           4
        .value_kind:     by_value
      - .offset:         32
        .size:           32
        .value_kind:     by_value
    .group_segment_fixed_size: 0
    .kernarg_segment_align: 8
    .kernarg_segment_size: 64
    .language:       OpenCL C
    .language_version:
      - 2
      - 0
    .max_flat_workgroup_size: 512
    .name:           _ZN2g811k_gemm128f8INS_6EpiResEEEvPKhS3_iiiT_
    .private_segment_fixed_size: 0
    .sgpr_count:     34
    .sgpr_spill_count: 0
    .symbol:         _ZN2g811k_gemm128f8INS_6EpiResEEEvPKhS3_iiiT_.kd
    .uniform_work_group_size: 1
    .uses_dynamic_stack: false
    .vgpr_count:     98
    .vgpr_spill_count: 0
    .wavefront_size: 64
  - .agpr_count:     0
    .args:
      - .address_space:  global
        .offset:         0
        .size:           8
        .value_kind:     global_buffer
      - .address_space:  global
        .offset:         8
        .size:           8
        .value_kind:     global_buffer
      - .offset:         16
        .size:           4
        .value_kind:     by_value
      - .offset:         20
        .size:           4
        .value_kind:     by_value
      - .offset:         24
        .size:           4
        .value_kind:     by_value
      - .offset:         32
        .size:           16
        .value_kind:     by_value
    .group_segment_fixed_size: 0
    .kernarg_segment_align: 8
    .kernarg_segment_size: 48
    .language:       OpenCL C
    .language_version:
      - 2
      - 0
    .max_flat_workgroup_size: 512
    .name:           _ZN2g811k_gemm128f8INS_5EpiQ8EEEvPKhS3_iiiT_
    .private_segment_fixed_size: 0
    .sgpr_count:     72
    .sgpr_spill_count: 0
    .symbol:         _ZN2g811k_gemm128f8INS_5EpiQ8EEEvPKhS3_iiiT_.kd
    .uniform_work_group_size: 1
    .uses_dynamic_stack: false
    .vgpr_count:     240
    .vgpr_spill_count: 0
    .wavefront_size: 64
  - .agpr_count:     0
    .args:
      - .address_space:  global
        .offset:         0
        .size:           8
        .value_kind:     global_buffer
      - .address_space:  global
        .offset:         8
        .size:           8
        .value_kind:     global_buffer
      - .address_space:  global
        .offset:         16
        .size:           8
        .value_kind:     global_buffer
      - .address_space:  global
        .offset:         24
        .size:           8
        .value_kind:     global_buffer
      - .address_space:  global
        .offset:         32
        .size:           8
        .value_kind:     global_buffer
    .group_segment_fixed_size: 0
    .kernarg_segment_align: 8
    .kernarg_segment_size: 40
    .language:       OpenCL C
    .language_version:
      - 2
      - 0
    .max_flat_workgroup_size: 512
    .name:           _Z6k_attnILi1024ELi2048ELi1024ELi1024ELi2048ELi1024ELb1ELb1EEvPKDF16_S1_S1_PKfPDF16_
    .private_segment_fixed_size: 0
    .sgpr_count:     52
    .sgpr_spill_count: 0
    .symbol:         _Z6k_attnILi1024ELi2048ELi1024ELi1024ELi2048ELi1024ELb1ELb1EEvPKDF16_S1_S1_PKfPDF16_.kd
    .uniform_work_group_size: 1
    .uses_dynamic_stack: false
    .vgpr_count:     224
    .vgpr_spill_count: 0
    .wavefront_size: 64
  - .agpr_count:     0
    .args:
      - .offset:         0
        .size:           56
        .value_kind:     by_value
      - .offset:         56
        .size:           72
        .value_kind:     by_value
      - .offset:         128
        .size:           176
        .value_kind:     by_value
      - .address_space:  global
        .offset:         304
        .size:           8
        .value_kind:     global_buffer
      - .offset:         312
        .size:           4
        .value_kind:     hidden_block_count_x
      - .offset:         316
        .size:           4
        .value_kind:     hidden_block_count_y
      - .offset:         320
        .size:           4
        .value_kind:     hidden_block_count_z
      - .offset:         324
        .size:           2
        .value_kind:     hidden_group_size_x
      - .offset:         326
        .size:           2
        .value_kind:     hidden_group_size_y
      - .offset:         328
        .size:           2
        .value_kind:     hidden_group_size_z
      - .offset:         330
        .size:           2
        .value_kind:     hidden_remainder_x
      - .offset:         332
        .size:           2
        .value_kind:     hidden_remainder_y
      - .offset:         334
        .size:           2
        .value_kind:     hidden_remainder_z
      - .offset:         352
        .size:           8
        .value_kind:     hidden_global_offset_x
      - .offset:         360
        .size:           8
        .value_kind:     hidden_global_offset_y
      - .offset:         368
        .size:           8
        .value_kind:     hidden_global_offset_z
      - .offset:         376
        .size:           2
        .value_kind:     hidden_grid_dims
      - .offset:         432
        .size:           4
        .value_kind:     hidden_dynamic_lds_size
    .group_segment_fixed_size: 0
    .kernarg_segment_align: 8
    .kernarg_segment_size: 568
    .language:       OpenCL C
    .language_version:
      - 2
      - 0
    .max_flat_workgroup_size: 512
    .name:           _Z6k_gemmIN3pg84EpiHILi1ELb0EEELb0EEvNS0_4GemmET_6WtTailPj
    .private_segment_fixed_size: 0
    .sgpr_count:     85
    .sgpr_spill_count: 0
    .symbol:         _Z6k_gemmIN3pg84EpiHILi1ELb0EEELb0EEvNS0_4GemmET_6WtTailPj.kd
    .uniform_work_group_size: 1
    .uses_dynamic_stack: false
    .vgpr_count:     242
    .vgpr_spill_count: 0
    .wavefront_size: 64
  - .agpr_count:     0
    .args:
      - .address_space:  global
        .offset:         0
        .size:           8
        .value_kind:     global_buffer
      - .address_space:  global
        .offset:         8
        .size:           8
        .value_kind:     global_buffer
      - .offset:         16
        .size:           4
        .value_kind:     by_value
      - .offset:         20
        .size:           4
        .value_kind:     by_value
      - .offset:         24
        .size:           4
        .value_kind:     by_value
      - .offset:         32
        .size:           32
        .value_kind:     by_value
    .group_segment_fixed_size: 0
    .kernarg_segment_align: 8
    .kernarg_segment_size: 64
    .language:       OpenCL C
    .language_version:
      - 2
      - 0
    .max_flat_workgroup_size: 512
    .name:           _ZN4g1289k_gemm128INS_8EpiRes16EEEvPKDF16_S3_iiiT_
    .private_segment_fixed_size: 0
    .sgpr_count:     35
    .sgpr_spill_count: 0
    .symbol:         _ZN4g1289k_gemm128INS_8EpiRes16EEEvPKDF16_S3_iiiT_.kd
    .uniform_work_group_size: 1
    .uses_dynamic_stack: false
    .vgpr_count:     112
    .vgpr_spill_count: 0
    .wavefront_size: 64
